# SwiGLU fp8 epilogues: output scale 8 folded exactly into the sigmoid denominator (fma 0.125e+0.125), one packed multiply fewer per output pair
# speedup vs baseline: 1.0071x; 1.0071x over previous
.LBB0_820:
	v_xor_b32_e32 v218, 16, v231
	v_and_b32_e32 v216, 64, v231
	v_add_u32_e32 v216, 64, v216
	v_xor_b32_e32 v217, 32, v231
	v_cmp_lt_i32_e32 vcc, v218, v216
	v_mov_b32_e32 v142, 0xbfb8aa3b
	v_mov_b32_e32 v143, 0x3e000000
	v_cndmask_b32_e32 v218, v231, v218, vcc
	v_cmp_lt_i32_e32 vcc, v217, v216
	v_lshlrev_b32_e32 v218, 2, v218
	v_mov_b32_e32 v144, 0x41000000
	v_cndmask_b32_e32 v217, v231, v217, vcc
	v_lshlrev_b32_e32 v217, 2, v217
	ds_bpermute_b32 v156, v218, v244
	ds_bpermute_b32 v157, v218, v245
	ds_bpermute_b32 v158, v218, v246
	ds_bpermute_b32 v159, v218, v247
	ds_bpermute_b32 v160, v218, v248
	ds_bpermute_b32 v161, v218, v249
	ds_bpermute_b32 v162, v218, v250
	ds_bpermute_b32 v163, v218, v251
	v_lshl_add_u32 v221, s52, 8, v149
	v_lshl_or_b32 v220, s63, 7, v153
	v_mad_u32_u24 v219, v221, s33, v220
	s_waitcnt lgkmcnt(7)
	v_add_f32_e32 v244, v244, v156
	ds_bpermute_b32 v156, v217, v244
	s_waitcnt lgkmcnt(7)
	v_add_f32_e32 v245, v245, v157
	ds_bpermute_b32 v157, v217, v245
	s_waitcnt lgkmcnt(7)
	v_add_f32_e32 v246, v246, v158
	ds_bpermute_b32 v158, v217, v246
	s_waitcnt lgkmcnt(7)
	v_add_f32_e32 v247, v247, v159
	ds_bpermute_b32 v159, v217, v247
	s_waitcnt lgkmcnt(7)
	v_add_f32_e32 v248, v248, v160
	ds_bpermute_b32 v160, v217, v248
	s_waitcnt lgkmcnt(7)
	v_add_f32_e32 v249, v249, v161
	ds_bpermute_b32 v161, v217, v249
	s_waitcnt lgkmcnt(7)
	v_add_f32_e32 v250, v250, v162
	ds_bpermute_b32 v162, v217, v250
	s_waitcnt lgkmcnt(7)
	v_add_f32_e32 v251, v251, v163
	ds_bpermute_b32 v163, v217, v251
	s_waitcnt lgkmcnt(7)
	v_add_f32_e32 v244, v244, v156
	v_fmamk_f32 v244, v244, 0x3a800000, v224
	s_waitcnt lgkmcnt(6)
	v_add_f32_e32 v245, v245, v157
	v_fmamk_f32 v245, v245, 0x3a800000, v224
	s_waitcnt lgkmcnt(5)
	v_add_f32_e32 v246, v246, v158
	v_fmamk_f32 v246, v246, 0x3a800000, v224
	s_waitcnt lgkmcnt(4)
	v_add_f32_e32 v247, v247, v159
	v_fmamk_f32 v247, v247, 0x3a800000, v224
	s_waitcnt lgkmcnt(3)
	v_add_f32_e32 v248, v248, v160
	v_fmamk_f32 v248, v248, 0x3a800000, v224
	s_waitcnt lgkmcnt(2)
	v_add_f32_e32 v249, v249, v161
	v_fmamk_f32 v249, v249, 0x3a800000, v224
	s_waitcnt lgkmcnt(1)
	v_add_f32_e32 v250, v250, v162
	v_fmamk_f32 v250, v250, 0x3a800000, v224
	s_waitcnt lgkmcnt(0)
	v_add_f32_e32 v251, v251, v163
	v_fmamk_f32 v251, v251, 0x3a800000, v224
	v_rsq_f32_e32 v244, v244
	v_rsq_f32_e32 v245, v245
	v_rsq_f32_e32 v246, v246
	v_rsq_f32_e32 v247, v247
	v_rsq_f32_e32 v248, v248
	v_rsq_f32_e32 v249, v249
	v_rsq_f32_e32 v250, v250
	v_rsq_f32_e32 v251, v251
	v_pk_mul_f32 v[156:157], v[126:127], v[244:245] op_sel_hi:[1,0]
	v_pk_mul_f32 v[158:159], v[128:129], v[244:245] op_sel_hi:[1,0]
	v_pk_mul_f32 v[160:161], v[118:119], v[244:245] op_sel_hi:[1,0]
	v_pk_mul_f32 v[162:163], v[156:157], v[142:143] op_sel_hi:[1,0]
	v_pk_mul_f32 v[170:171], v[158:159], v[142:143] op_sel_hi:[1,0]
	v_pk_mul_f32 v[172:173], v[160:161], v[142:143] op_sel_hi:[1,0]
	v_exp_f32_e32 v162, v162
	v_pk_mul_f32 v[174:175], v[120:121], v[244:245] op_sel_hi:[1,0]
	v_exp_f32_e32 v170, v170
	v_pk_mul_f32 v[176:177], v[110:111], v[244:245] op_sel:[0,1] op_sel_hi:[1,1]
	v_exp_f32_e32 v172, v172
	v_pk_mul_f32 v[178:179], v[174:175], v[142:143] op_sel_hi:[1,0]
	v_pk_mul_f32 v[180:181], v[176:177], v[142:143] op_sel_hi:[1,0]
	v_pk_mul_f32 v[182:183], v[112:113], v[244:245] op_sel:[0,1] op_sel_hi:[1,1]
	v_exp_f32_e32 v178, v178
	v_pk_mul_f32 v[184:185], v[102:103], v[244:245] op_sel:[0,1] op_sel_hi:[1,1]
	v_exp_f32_e32 v163, v163
	v_pk_mul_f32 v[186:187], v[182:183], v[142:143] op_sel_hi:[1,0]
	v_exp_f32_e32 v171, v171
	v_pk_mul_f32 v[188:189], v[184:185], v[142:143] op_sel_hi:[1,0]
	v_exp_f32_e32 v173, v173
	v_pk_mul_f32 v[190:191], v[104:105], v[244:245] op_sel:[0,1] op_sel_hi:[1,1]
	v_exp_f32_e32 v179, v179
	v_pk_mul_f32 v[192:193], v[122:123], v[244:245] op_sel_hi:[1,0]
	v_pk_fma_f32 v[162:163], v[162:163], v[142:143], v[142:143] op_sel:[0,1,1] op_sel_hi:[1,1,1]
	v_exp_f32_e32 v180, v180
	v_pk_fma_f32 v[170:171], v[170:171], v[142:143], v[142:143] op_sel:[0,1,1] op_sel_hi:[1,1,1]
	v_rcp_f32_e32 v162, v162
	v_pk_fma_f32 v[172:173], v[172:173], v[142:143], v[142:143] op_sel:[0,1,1] op_sel_hi:[1,1,1]
	v_rcp_f32_e32 v170, v170
	v_pk_fma_f32 v[178:179], v[178:179], v[142:143], v[142:143] op_sel:[0,1,1] op_sel_hi:[1,1,1]
	v_rcp_f32_e32 v172, v172
	v_pk_mul_f32 v[194:195], v[190:191], v[142:143] op_sel_hi:[1,0]
	v_rcp_f32_e32 v178, v178
	v_pk_mul_f32 v[192:193], v[192:193], v[156:157]
	v_exp_f32_e32 v186, v186
	v_pk_mul_f32 v[156:157], v[124:125], v[244:245] op_sel_hi:[1,0]
	v_exp_f32_e32 v188, v188
	v_pk_mul_f32 v[196:197], v[114:115], v[244:245] op_sel_hi:[1,0]
	v_rcp_f32_e32 v163, v163
	v_pk_mul_f32 v[198:199], v[94:95], v[246:247] op_sel_hi:[1,0]
	v_exp_f32_e32 v194, v194
	v_pk_mul_f32 v[156:157], v[156:157], v[158:159]
	v_rcp_f32_e32 v171, v171
	v_pk_mul_f32 v[196:197], v[196:197], v[160:161]
	v_rcp_f32_e32 v173, v173
	v_pk_mul_f32 v[158:159], v[116:117], v[244:245] op_sel_hi:[1,0]
	v_exp_f32_e32 v181, v181
	v_pk_mul_f32 v[192:193], v[192:193], v[162:163]
	v_rcp_f32_e32 v179, v179
	v_pk_mul_f32 v[160:161], v[198:199], v[142:143] op_sel_hi:[1,0]
	v_exp_f32_e32 v187, v187
	v_med3_f32 v192, v192, s87, v227
	v_exp_f32_e32 v189, v189
	v_pk_mul_f32 v[156:157], v[156:157], v[170:171]
	v_exp_f32_e32 v195, v195
	v_pk_mul_f32 v[196:197], v[196:197], v[172:173]
	v_pk_fma_f32 v[180:181], v[180:181], v[142:143], v[142:143] op_sel:[0,1,1] op_sel_hi:[1,1,1]
	v_med3_f32 v193, v193, s87, v227
	v_med3_f32 v156, v156, s87, v227
	v_med3_f32 v196, v196, s87, v227
	v_rcp_f32_e32 v180, v180
	v_pk_fma_f32 v[186:187], v[186:187], v[142:143], v[142:143] op_sel:[0,1,1] op_sel_hi:[1,1,1]
	v_pk_fma_f32 v[188:189], v[188:189], v[142:143], v[142:143] op_sel:[0,1,1] op_sel_hi:[1,1,1]
	v_pk_mul_f32 v[162:163], v[96:97], v[246:247] op_sel_hi:[1,0]
	v_pk_mul_f32 v[170:171], v[86:87], v[246:247] op_sel_hi:[1,0]
	v_cvt_pk_fp8_f32 v172, v192, v193
	v_med3_f32 v157, v157, s87, v227
	v_med3_f32 v197, v197, s87, v227
	v_pk_mul_f32 v[158:159], v[158:159], v[174:175]
	v_rcp_f32_e32 v186, v186
	v_pk_fma_f32 v[194:195], v[194:195], v[142:143], v[142:143] op_sel:[0,1,1] op_sel_hi:[1,1,1]
	v_pk_mul_f32 v[158:159], v[158:159], v[178:179]
	v_rcp_f32_e32 v188, v188
	v_pk_mul_f32 v[174:175], v[162:163], v[142:143] op_sel_hi:[1,0]
	v_med3_f32 v158, v158, s87, v227
	v_exp_f32_e32 v160, v160
	v_pk_mul_f32 v[178:179], v[170:171], v[142:143] op_sel_hi:[1,0]
	v_pk_mul_f32 v[192:193], v[88:89], v[246:247] op_sel_hi:[1,0]
	v_cvt_pk_fp8_f32 v172, v156, v157 op_sel:[0,0,1]
	v_cvt_pk_fp8_f32 v173, v196, v197
	v_med3_f32 v159, v159, s87, v227
	v_rcp_f32_e32 v194, v194
	v_pk_mul_f32 v[156:157], v[192:193], v[142:143] op_sel_hi:[1,0]
	v_exp_f32_e32 v174, v174
	v_cvt_pk_fp8_f32 v173, v158, v159 op_sel:[0,0,1]
	v_exp_f32_e32 v178, v178
	v_pk_mul_f32 v[158:159], v[106:107], v[244:245] op_sel:[0,1] op_sel_hi:[1,1]
	v_rcp_f32_e32 v181, v181
	global_store_dwordx2 v219, v[172:173], s[26:27]
	v_exp_f32_e32 v156, v156
	v_pk_mul_f32 v[158:159], v[158:159], v[176:177]
	v_rcp_f32_e32 v187, v187
	v_pk_mul_f32 v[172:173], v[108:109], v[244:245] op_sel:[0,1] op_sel_hi:[1,1]
	v_rcp_f32_e32 v189, v189
	v_pk_mul_f32 v[176:177], v[98:99], v[244:245] op_sel:[0,1] op_sel_hi:[1,1]
	v_exp_f32_e32 v161, v161
	v_pk_mul_f32 v[158:159], v[158:159], v[180:181]
	v_rcp_f32_e32 v195, v195
	v_pk_mul_f32 v[180:181], v[78:79], v[246:247] op_sel:[0,1] op_sel_hi:[1,1]
	v_exp_f32_e32 v175, v175
	v_med3_f32 v158, v158, s87, v227
	v_exp_f32_e32 v179, v179
	v_pk_mul_f32 v[172:173], v[172:173], v[182:183]
	v_exp_f32_e32 v157, v157
	v_pk_fma_f32 v[160:161], v[160:161], v[142:143], v[142:143] op_sel:[0,1,1] op_sel_hi:[1,1,1]
	v_pk_mul_f32 v[172:173], v[172:173], v[186:187]
	v_med3_f32 v159, v159, s87, v227
	v_pk_mul_f32 v[176:177], v[176:177], v[184:185]
	v_med3_f32 v172, v172, s87, v227
	v_pk_mul_f32 v[182:183], v[100:101], v[244:245] op_sel:[0,1] op_sel_hi:[1,1]
	v_pk_mul_f32 v[176:177], v[176:177], v[188:189]
	v_rcp_f32_e32 v160, v160
	v_pk_fma_f32 v[174:175], v[174:175], v[142:143], v[142:143] op_sel:[0,1,1] op_sel_hi:[1,1,1]
	v_med3_f32 v176, v176, s87, v227
	v_pk_fma_f32 v[178:179], v[178:179], v[142:143], v[142:143] op_sel:[0,1,1] op_sel_hi:[1,1,1]
	v_pk_mul_f32 v[184:185], v[180:181], v[142:143] op_sel_hi:[1,0]
	v_pk_mul_f32 v[186:187], v[80:81], v[246:247] op_sel:[0,1] op_sel_hi:[1,1]
	v_pk_mul_f32 v[188:189], v[70:71], v[246:247] op_sel:[0,1] op_sel_hi:[1,1]
	v_cvt_pk_fp8_f32 v158, v158, v159
	v_med3_f32 v173, v173, s87, v227
	v_med3_f32 v177, v177, s87, v227
	v_pk_mul_f32 v[182:183], v[182:183], v[190:191]
	v_rcp_f32_e32 v174, v174
	v_pk_fma_f32 v[156:157], v[156:157], v[142:143], v[142:143] op_sel:[0,1,1] op_sel_hi:[1,1,1]
	v_pk_mul_f32 v[182:183], v[182:183], v[194:195]
	v_rcp_f32_e32 v178, v178
	v_pk_mul_f32 v[190:191], v[186:187], v[142:143] op_sel_hi:[1,0]
	v_med3_f32 v182, v182, s87, v227
	v_exp_f32_e32 v184, v184
	v_pk_mul_f32 v[194:195], v[188:189], v[142:143] op_sel_hi:[1,0]
	v_pk_mul_f32 v[196:197], v[72:73], v[246:247] op_sel:[0,1] op_sel_hi:[1,1]
	v_cvt_pk_fp8_f32 v158, v172, v173 op_sel:[0,0,1]
	v_cvt_pk_fp8_f32 v159, v176, v177
	v_med3_f32 v183, v183, s87, v227
	v_rcp_f32_e32 v156, v156
	v_pk_mul_f32 v[172:173], v[196:197], v[142:143] op_sel_hi:[1,0]
	v_exp_f32_e32 v190, v190
	v_cvt_pk_fp8_f32 v159, v182, v183 op_sel:[0,0,1]
	v_exp_f32_e32 v194, v194
	v_pk_mul_f32 v[176:177], v[90:91], v[246:247] op_sel_hi:[1,0]
	v_rcp_f32_e32 v161, v161
	v_pk_mul_f32 v[182:183], v[92:93], v[246:247] op_sel_hi:[1,0]
	v_exp_f32_e32 v172, v172
	v_pk_mul_f32 v[176:177], v[176:177], v[198:199]
	v_rcp_f32_e32 v175, v175
	v_pk_mul_f32 v[198:199], v[82:83], v[246:247] op_sel_hi:[1,0]
	v_rcp_f32_e32 v179, v179
	v_pk_mul_f32 v[200:201], v[62:63], v[248:249] op_sel_hi:[1,0]
	v_exp_f32_e32 v185, v185
	v_pk_mul_f32 v[176:177], v[176:177], v[160:161]
	v_rcp_f32_e32 v157, v157
	v_pk_mul_f32 v[182:183], v[182:183], v[162:163]
	v_exp_f32_e32 v191, v191
	v_med3_f32 v176, v176, s87, v227
	v_exp_f32_e32 v195, v195
	v_pk_mul_f32 v[182:183], v[182:183], v[174:175]
	v_exp_f32_e32 v173, v173
	v_pk_fma_f32 v[184:185], v[184:185], v[142:143], v[142:143] op_sel:[0,1,1] op_sel_hi:[1,1,1]
	v_med3_f32 v177, v177, s87, v227
	v_med3_f32 v182, v182, s87, v227
	v_pk_mul_f32 v[198:199], v[198:199], v[170:171]
	v_pk_mul_f32 v[160:161], v[84:85], v[246:247] op_sel_hi:[1,0]
	v_rcp_f32_e32 v184, v184
	v_pk_mul_f32 v[198:199], v[198:199], v[178:179]
	v_pk_fma_f32 v[190:191], v[190:191], v[142:143], v[142:143] op_sel:[0,1,1] op_sel_hi:[1,1,1]
	v_pk_fma_f32 v[194:195], v[194:195], v[142:143], v[142:143] op_sel:[0,1,1] op_sel_hi:[1,1,1]
	v_med3_f32 v198, v198, s87, v227
	v_pk_mul_f32 v[162:163], v[200:201], v[142:143] op_sel_hi:[1,0]
	v_pk_mul_f32 v[170:171], v[64:65], v[248:249] op_sel_hi:[1,0]
	v_pk_mul_f32 v[174:175], v[54:55], v[248:249] op_sel_hi:[1,0]
	v_cvt_pk_fp8_f32 v176, v176, v177
	v_med3_f32 v183, v183, s87, v227
	v_med3_f32 v199, v199, s87, v227
	v_pk_mul_f32 v[160:161], v[160:161], v[192:193]
	v_rcp_f32_e32 v190, v190
	v_pk_fma_f32 v[172:173], v[172:173], v[142:143], v[142:143] op_sel:[0,1,1] op_sel_hi:[1,1,1]
	v_pk_mul_f32 v[160:161], v[160:161], v[156:157]
	v_rcp_f32_e32 v194, v194
	v_pk_mul_f32 v[156:157], v[170:171], v[142:143] op_sel_hi:[1,0]
	v_med3_f32 v160, v160, s87, v227
	v_exp_f32_e32 v162, v162
	v_pk_mul_f32 v[178:179], v[174:175], v[142:143] op_sel_hi:[1,0]
	v_pk_mul_f32 v[192:193], v[56:57], v[248:249] op_sel_hi:[1,0]
	v_cvt_pk_fp8_f32 v176, v182, v183 op_sel:[0,0,1]
	v_cvt_pk_fp8_f32 v177, v198, v199
	v_med3_f32 v161, v161, s87, v227
	v_rcp_f32_e32 v172, v172
	v_pk_mul_f32 v[182:183], v[192:193], v[142:143] op_sel_hi:[1,0]
	v_exp_f32_e32 v156, v156
	v_add_u32_e32 v198, 0xe000, v219
	v_exp_f32_e32 v178, v178
	v_cvt_pk_fp8_f32 v177, v160, v161 op_sel:[0,0,1]
	global_store_dwordx2 v198, v[158:159], s[26:27]
	v_rcp_f32_e32 v185, v185
	v_pk_mul_f32 v[158:159], v[74:75], v[246:247] op_sel:[0,1] op_sel_hi:[1,1]
	v_exp_f32_e32 v182, v182
	v_pk_mul_f32 v[160:161], v[76:77], v[246:247] op_sel:[0,1] op_sel_hi:[1,1]
	v_rcp_f32_e32 v191, v191
	v_pk_mul_f32 v[158:159], v[158:159], v[180:181]
	v_rcp_f32_e32 v195, v195
	v_pk_mul_f32 v[180:181], v[66:67], v[246:247] op_sel:[0,1] op_sel_hi:[1,1]
	v_exp_f32_e32 v163, v163
	v_pk_mul_f32 v[158:159], v[158:159], v[184:185]
	v_rcp_f32_e32 v173, v173
	v_pk_mul_f32 v[184:185], v[46:47], v[248:249] op_sel:[0,1] op_sel_hi:[1,1]
	v_exp_f32_e32 v157, v157
	v_med3_f32 v158, v158, s87, v227
	v_exp_f32_e32 v179, v179
	v_pk_mul_f32 v[160:161], v[160:161], v[186:187]
	v_exp_f32_e32 v183, v183
	v_pk_fma_f32 v[162:163], v[162:163], v[142:143], v[142:143] op_sel:[0,1,1] op_sel_hi:[1,1,1]
	v_pk_mul_f32 v[160:161], v[160:161], v[190:191]
	v_med3_f32 v159, v159, s87, v227
	v_pk_mul_f32 v[180:181], v[180:181], v[188:189]
	v_med3_f32 v160, v160, s87, v227
	v_pk_mul_f32 v[186:187], v[68:69], v[246:247] op_sel:[0,1] op_sel_hi:[1,1]
	v_pk_mul_f32 v[180:181], v[180:181], v[194:195]
	v_rcp_f32_e32 v162, v162
	v_pk_fma_f32 v[156:157], v[156:157], v[142:143], v[142:143] op_sel:[0,1,1] op_sel_hi:[1,1,1]
	v_med3_f32 v180, v180, s87, v227
	v_pk_fma_f32 v[178:179], v[178:179], v[142:143], v[142:143] op_sel:[0,1,1] op_sel_hi:[1,1,1]
	v_pk_mul_f32 v[188:189], v[184:185], v[142:143] op_sel_hi:[1,0]
	v_pk_mul_f32 v[190:191], v[48:49], v[248:249] op_sel:[0,1] op_sel_hi:[1,1]
	v_pk_mul_f32 v[194:195], v[38:39], v[248:249] op_sel:[0,1] op_sel_hi:[1,1]
	v_cvt_pk_fp8_f32 v158, v158, v159
	v_med3_f32 v161, v161, s87, v227
	v_med3_f32 v181, v181, s87, v227
	v_pk_mul_f32 v[186:187], v[186:187], v[196:197]
	v_rcp_f32_e32 v156, v156
	v_pk_fma_f32 v[182:183], v[182:183], v[142:143], v[142:143] op_sel:[0,1,1] op_sel_hi:[1,1,1]
	v_pk_mul_f32 v[186:187], v[186:187], v[172:173]
	v_rcp_f32_e32 v178, v178
	v_pk_mul_f32 v[172:173], v[190:191], v[142:143] op_sel_hi:[1,0]
	v_med3_f32 v186, v186, s87, v227
	v_exp_f32_e32 v188, v188
	v_pk_mul_f32 v[196:197], v[194:195], v[142:143] op_sel_hi:[1,0]
	v_pk_mul_f32 v[198:199], v[40:41], v[248:249] op_sel:[0,1] op_sel_hi:[1,1]
	v_cvt_pk_fp8_f32 v158, v160, v161 op_sel:[0,0,1]
	v_cvt_pk_fp8_f32 v159, v180, v181
	v_med3_f32 v187, v187, s87, v227
	v_rcp_f32_e32 v182, v182
	v_pk_mul_f32 v[160:161], v[198:199], v[142:143] op_sel_hi:[1,0]
	v_exp_f32_e32 v172, v172
	v_add_u32_e32 v180, 0x1c000, v219
	v_exp_f32_e32 v196, v196
	v_cvt_pk_fp8_f32 v159, v186, v187 op_sel:[0,0,1]
	global_store_dwordx2 v180, v[176:177], s[26:27]
	v_rcp_f32_e32 v163, v163
	v_pk_mul_f32 v[176:177], v[58:59], v[248:249] op_sel_hi:[1,0]
	v_exp_f32_e32 v160, v160
	v_pk_mul_f32 v[180:181], v[60:61], v[248:249] op_sel_hi:[1,0]
	v_rcp_f32_e32 v157, v157
	v_pk_mul_f32 v[176:177], v[176:177], v[200:201]
	v_rcp_f32_e32 v179, v179
	v_pk_mul_f32 v[186:187], v[50:51], v[248:249] op_sel_hi:[1,0]
	v_exp_f32_e32 v189, v189
	v_pk_mul_f32 v[176:177], v[176:177], v[162:163]
	v_rcp_f32_e32 v183, v183
	v_pk_mul_f32 v[162:163], v[30:31], v[250:251] op_sel_hi:[1,0]
	v_exp_f32_e32 v173, v173
	v_med3_f32 v176, v176, s87, v227
	v_exp_f32_e32 v197, v197
	v_pk_mul_f32 v[180:181], v[180:181], v[170:171]
	v_exp_f32_e32 v161, v161
	v_pk_fma_f32 v[188:189], v[188:189], v[142:143], v[142:143] op_sel:[0,1,1] op_sel_hi:[1,1,1]
	v_pk_mul_f32 v[180:181], v[180:181], v[156:157]
	v_med3_f32 v177, v177, s87, v227
	v_pk_mul_f32 v[186:187], v[186:187], v[174:175]
	v_med3_f32 v180, v180, s87, v227
	v_pk_mul_f32 v[156:157], v[52:53], v[248:249] op_sel_hi:[1,0]
	v_pk_mul_f32 v[186:187], v[186:187], v[178:179]
	v_rcp_f32_e32 v188, v188
	v_pk_fma_f32 v[172:173], v[172:173], v[142:143], v[142:143] op_sel:[0,1,1] op_sel_hi:[1,1,1]
	v_med3_f32 v186, v186, s87, v227
	v_pk_fma_f32 v[196:197], v[196:197], v[142:143], v[142:143] op_sel:[0,1,1] op_sel_hi:[1,1,1]
	v_pk_mul_f32 v[170:171], v[162:163], v[142:143] op_sel_hi:[1,0]
	v_pk_mul_f32 v[174:175], v[32:33], v[250:251] op_sel_hi:[1,0]
	v_pk_mul_f32 v[178:179], v[22:23], v[250:251] op_sel_hi:[1,0]
	v_cvt_pk_fp8_f32 v176, v176, v177
	v_med3_f32 v181, v181, s87, v227
	v_med3_f32 v187, v187, s87, v227
	v_pk_mul_f32 v[156:157], v[156:157], v[192:193]
	v_rcp_f32_e32 v172, v172
	v_pk_fma_f32 v[160:161], v[160:161], v[142:143], v[142:143] op_sel:[0,1,1] op_sel_hi:[1,1,1]
	v_pk_mul_f32 v[156:157], v[156:157], v[182:183]
	v_rcp_f32_e32 v196, v196
	v_pk_mul_f32 v[182:183], v[174:175], v[142:143] op_sel_hi:[1,0]
	v_med3_f32 v156, v156, s87, v227
	v_exp_f32_e32 v170, v170
	v_pk_mul_f32 v[192:193], v[178:179], v[142:143] op_sel_hi:[1,0]
	v_pk_mul_f32 v[200:201], v[24:25], v[250:251] op_sel_hi:[1,0]
	v_cvt_pk_fp8_f32 v176, v180, v181 op_sel:[0,0,1]
	v_cvt_pk_fp8_f32 v177, v186, v187
	v_med3_f32 v157, v157, s87, v227
	v_rcp_f32_e32 v160, v160
	v_pk_mul_f32 v[180:181], v[200:201], v[142:143] op_sel_hi:[1,0]
	v_exp_f32_e32 v182, v182
	v_add_u32_e32 v186, 0x2a000, v219
	v_exp_f32_e32 v192, v192
	v_cvt_pk_fp8_f32 v177, v156, v157 op_sel:[0,0,1]
	global_store_dwordx2 v186, v[158:159], s[26:27]
	v_rcp_f32_e32 v189, v189
	v_pk_mul_f32 v[156:157], v[42:43], v[248:249] op_sel:[0,1] op_sel_hi:[1,1]
	v_exp_f32_e32 v180, v180
	v_pk_mul_f32 v[158:159], v[44:45], v[248:249] op_sel:[0,1] op_sel_hi:[1,1]
	v_rcp_f32_e32 v173, v173
	v_pk_mul_f32 v[156:157], v[156:157], v[184:185]
	v_rcp_f32_e32 v197, v197
	v_pk_mul_f32 v[184:185], v[34:35], v[248:249] op_sel:[0,1] op_sel_hi:[1,1]
	v_exp_f32_e32 v171, v171
	v_pk_mul_f32 v[156:157], v[156:157], v[188:189]
	v_rcp_f32_e32 v161, v161
	v_pk_mul_f32 v[186:187], v[14:15], v[250:251] op_sel:[0,1] op_sel_hi:[1,1]
	v_exp_f32_e32 v183, v183
	v_med3_f32 v156, v156, s87, v227
	v_exp_f32_e32 v193, v193
	v_pk_mul_f32 v[158:159], v[158:159], v[190:191]
	v_exp_f32_e32 v181, v181
	v_pk_fma_f32 v[170:171], v[170:171], v[142:143], v[142:143] op_sel:[0,1,1] op_sel_hi:[1,1,1]
	v_pk_mul_f32 v[158:159], v[158:159], v[172:173]
	v_med3_f32 v157, v157, s87, v227
	v_pk_mul_f32 v[184:185], v[184:185], v[194:195]
	v_med3_f32 v158, v158, s87, v227
	v_pk_mul_f32 v[172:173], v[36:37], v[248:249] op_sel:[0,1] op_sel_hi:[1,1]
	v_pk_mul_f32 v[184:185], v[184:185], v[196:197]
	v_rcp_f32_e32 v170, v170
	v_pk_fma_f32 v[182:183], v[182:183], v[142:143], v[142:143] op_sel:[0,1,1] op_sel_hi:[1,1,1]
	v_med3_f32 v184, v184, s87, v227
	v_pk_fma_f32 v[192:193], v[192:193], v[142:143], v[142:143] op_sel:[0,1,1] op_sel_hi:[1,1,1]
	v_pk_mul_f32 v[188:189], v[186:187], v[142:143] op_sel_hi:[1,0]
	v_pk_mul_f32 v[190:191], v[16:17], v[250:251] op_sel:[0,1] op_sel_hi:[1,1]
	v_pk_mul_f32 v[194:195], v[6:7], v[250:251] op_sel:[0,1] op_sel_hi:[1,1]
	v_cvt_pk_fp8_f32 v156, v156, v157
	v_med3_f32 v159, v159, s87, v227
	v_med3_f32 v185, v185, s87, v227
	v_pk_mul_f32 v[172:173], v[172:173], v[198:199]
	v_rcp_f32_e32 v182, v182
	v_pk_fma_f32 v[180:181], v[180:181], v[142:143], v[142:143] op_sel:[0,1,1] op_sel_hi:[1,1,1]
	v_pk_mul_f32 v[172:173], v[172:173], v[160:161]
	v_rcp_f32_e32 v192, v192
	v_pk_mul_f32 v[160:161], v[190:191], v[142:143] op_sel_hi:[1,0]
	v_med3_f32 v172, v172, s87, v227
	v_exp_f32_e32 v188, v188
	v_pk_mul_f32 v[196:197], v[194:195], v[142:143] op_sel_hi:[1,0]
	v_pk_mul_f32 v[198:199], v[8:9], v[250:251] op_sel:[0,1] op_sel_hi:[1,1]
	v_cvt_pk_fp8_f32 v156, v158, v159 op_sel:[0,0,1]
	v_cvt_pk_fp8_f32 v157, v184, v185
	v_med3_f32 v173, v173, s87, v227
	v_rcp_f32_e32 v180, v180
	v_pk_mul_f32 v[158:159], v[198:199], v[142:143] op_sel_hi:[1,0]
	v_exp_f32_e32 v160, v160
	v_add_u32_e32 v184, 0x70000, v219
	v_exp_f32_e32 v196, v196
	v_cvt_pk_fp8_f32 v157, v172, v173 op_sel:[0,0,1]
	global_store_dwordx2 v184, v[176:177], s[26:27]
	v_rcp_f32_e32 v171, v171
	v_pk_mul_f32 v[172:173], v[26:27], v[250:251] op_sel_hi:[1,0]
	v_exp_f32_e32 v158, v158
	v_pk_mul_f32 v[176:177], v[28:29], v[250:251] op_sel_hi:[1,0]
	v_rcp_f32_e32 v183, v183
	v_pk_mul_f32 v[172:173], v[172:173], v[162:163]
	v_rcp_f32_e32 v193, v193
	v_pk_mul_f32 v[162:163], v[18:19], v[250:251] op_sel_hi:[1,0]
	v_exp_f32_e32 v189, v189
	v_pk_mul_f32 v[172:173], v[172:173], v[170:171]
	v_rcp_f32_e32 v181, v181
	v_pk_mul_f32 v[176:177], v[176:177], v[174:175]
	v_exp_f32_e32 v161, v161
	v_med3_f32 v172, v172, s87, v227
	v_exp_f32_e32 v197, v197
	v_pk_mul_f32 v[176:177], v[176:177], v[182:183]
	v_exp_f32_e32 v159, v159
	v_pk_fma_f32 v[188:189], v[188:189], v[142:143], v[142:143] op_sel:[0,1,1] op_sel_hi:[1,1,1]
	v_med3_f32 v173, v173, s87, v227
	v_med3_f32 v176, v176, s87, v227
	v_pk_mul_f32 v[162:163], v[162:163], v[178:179]
	v_pk_mul_f32 v[170:171], v[20:21], v[250:251] op_sel_hi:[1,0]
	v_rcp_f32_e32 v188, v188
	v_pk_mul_f32 v[162:163], v[162:163], v[192:193]
	v_pk_fma_f32 v[160:161], v[160:161], v[142:143], v[142:143] op_sel:[0,1,1] op_sel_hi:[1,1,1]
	v_pk_fma_f32 v[196:197], v[196:197], v[142:143], v[142:143] op_sel:[0,1,1] op_sel_hi:[1,1,1]
	v_med3_f32 v162, v162, s87, v227
	v_cvt_pk_fp8_f32 v172, v172, v173
	v_med3_f32 v177, v177, s87, v227
	v_med3_f32 v163, v163, s87, v227
	v_pk_mul_f32 v[170:171], v[170:171], v[200:201]
	v_rcp_f32_e32 v160, v160
	v_pk_fma_f32 v[158:159], v[158:159], v[142:143], v[142:143] op_sel:[0,1,1] op_sel_hi:[1,1,1]
	v_pk_mul_f32 v[170:171], v[170:171], v[180:181]
	v_rcp_f32_e32 v196, v196
	v_cvt_pk_fp8_f32 v172, v176, v177 op_sel:[0,0,1]
	v_med3_f32 v170, v170, s87, v227
	v_cvt_pk_fp8_f32 v173, v162, v163
	v_rcp_f32_e32 v158, v158
	v_med3_f32 v171, v171, s87, v227
	v_add_u32_e32 v162, 0x7e000, v219
	v_rcp_f32_e32 v189, v189
	v_cvt_pk_fp8_f32 v173, v170, v171 op_sel:[0,0,1]
	global_store_dwordx2 v162, v[156:157], s[26:27]
	v_rcp_f32_e32 v161, v161
	v_pk_mul_f32 v[156:157], v[10:11], v[250:251] op_sel:[0,1] op_sel_hi:[1,1]
	v_rcp_f32_e32 v197, v197
	v_pk_mul_f32 v[162:163], v[12:13], v[250:251] op_sel:[0,1] op_sel_hi:[1,1]
	v_rcp_f32_e32 v159, v159
	v_pk_mul_f32 v[156:157], v[156:157], v[186:187]
	v_pk_mul_f32 v[170:171], v[2:3], v[250:251] op_sel:[0,1] op_sel_hi:[1,1]
	v_pk_mul_f32 v[162:163], v[162:163], v[190:191]
	v_pk_mul_f32 v[156:157], v[156:157], v[188:189]
	v_pk_mul_f32 v[170:171], v[170:171], v[194:195]
	v_pk_mul_f32 v[162:163], v[162:163], v[160:161]
	v_med3_f32 v156, v156, s87, v227
	v_pk_mul_f32 v[170:171], v[170:171], v[196:197]
	v_med3_f32 v162, v162, s87, v227
	v_med3_f32 v157, v157, s87, v227
	v_med3_f32 v170, v170, s87, v227
	v_pk_mul_f32 v[160:161], v[4:5], v[250:251] op_sel:[0,1] op_sel_hi:[1,1]
	v_cvt_pk_fp8_f32 v156, v156, v157
	v_med3_f32 v163, v163, s87, v227
	v_med3_f32 v171, v171, s87, v227
	v_pk_mul_f32 v[160:161], v[160:161], v[198:199]
	v_cvt_pk_fp8_f32 v156, v162, v163 op_sel:[0,0,1]
	v_cvt_pk_fp8_f32 v157, v170, v171
	v_pk_mul_f32 v[160:161], v[160:161], v[158:159]
	v_add_u32_e32 v158, 0x8c000, v219
	v_add_u32_e32 v159, 0x9a000, v219
	v_med3_f32 v160, v160, s87, v227
	global_store_dwordx2 v158, v[172:173], s[26:27]
	v_med3_f32 v161, v161, s87, v227
	v_cvt_pk_fp8_f32 v157, v160, v161 op_sel:[0,0,1]
	global_store_dwordx2 v159, v[156:157], s[26:27]
	s_andn2_b64 vcc, exec, s[46:47]
	s_mov_b64 s[46:47], -1
	s_cbranch_vccnz .LBB0_807
	s_andn2_b64 vcc, exec, s[30:31]
	s_cbranch_vccnz .LBB0_806
	s_barrier
	s_branch .LBB0_806

.LBB0_845:
	v_xor_b32_e32 v240, 16, v231
	v_and_b32_e32 v238, 64, v231
	v_add_u32_e32 v238, 64, v238
	v_xor_b32_e32 v239, 32, v231
	v_cmp_lt_i32_e32 vcc, v240, v238
	v_mov_b32_e32 v2, 0xbfb8aa3b
	v_mov_b32_e32 v3, 0x3e000000
	v_cndmask_b32_e32 v240, v231, v240, vcc
	v_cmp_lt_i32_e32 vcc, v239, v238
	v_lshlrev_b32_e32 v240, 2, v240
	v_mov_b32_e32 v4, 0x41000000
	v_cndmask_b32_e32 v239, v231, v239, vcc
	v_lshlrev_b32_e32 v239, 2, v239
	ds_bpermute_b32 v6, v240, v244
	ds_bpermute_b32 v7, v240, v245
	ds_bpermute_b32 v8, v240, v246
	ds_bpermute_b32 v9, v240, v247
	ds_bpermute_b32 v10, v240, v248
	ds_bpermute_b32 v11, v240, v249
	ds_bpermute_b32 v12, v240, v250
	ds_bpermute_b32 v13, v240, v251
	v_lshl_add_u32 v243, s50, 8, v195
	v_lshl_or_b32 v242, s61, 7, v197
	v_mad_u32_u24 v241, v243, s33, v242
	s_waitcnt lgkmcnt(7)
	v_add_f32_e32 v244, v244, v6
	ds_bpermute_b32 v6, v239, v244
	s_waitcnt lgkmcnt(7)
	v_add_f32_e32 v245, v245, v7
	ds_bpermute_b32 v7, v239, v245
	s_waitcnt lgkmcnt(7)
	v_add_f32_e32 v246, v246, v8
	ds_bpermute_b32 v8, v239, v246
	s_waitcnt lgkmcnt(7)
	v_add_f32_e32 v247, v247, v9
	ds_bpermute_b32 v9, v239, v247
	s_waitcnt lgkmcnt(7)
	v_add_f32_e32 v248, v248, v10
	ds_bpermute_b32 v10, v239, v248
	s_waitcnt lgkmcnt(7)
	v_add_f32_e32 v249, v249, v11
	ds_bpermute_b32 v11, v239, v249
	s_waitcnt lgkmcnt(7)
	v_add_f32_e32 v250, v250, v12
	ds_bpermute_b32 v12, v239, v250
	s_waitcnt lgkmcnt(7)
	v_add_f32_e32 v251, v251, v13
	ds_bpermute_b32 v13, v239, v251
	s_waitcnt lgkmcnt(7)
	v_add_f32_e32 v244, v244, v6
	v_fmamk_f32 v244, v244, 0x3a800000, v224
	s_waitcnt lgkmcnt(6)
	v_add_f32_e32 v245, v245, v7
	v_fmamk_f32 v245, v245, 0x3a800000, v224
	s_waitcnt lgkmcnt(5)
	v_add_f32_e32 v246, v246, v8
	v_fmamk_f32 v246, v246, 0x3a800000, v224
	s_waitcnt lgkmcnt(4)
	v_add_f32_e32 v247, v247, v9
	v_fmamk_f32 v247, v247, 0x3a800000, v224
	s_waitcnt lgkmcnt(3)
	v_add_f32_e32 v248, v248, v10
	v_fmamk_f32 v248, v248, 0x3a800000, v224
	s_waitcnt lgkmcnt(2)
	v_add_f32_e32 v249, v249, v11
	v_fmamk_f32 v249, v249, 0x3a800000, v224
	s_waitcnt lgkmcnt(1)
	v_add_f32_e32 v250, v250, v12
	v_fmamk_f32 v250, v250, 0x3a800000, v224
	s_waitcnt lgkmcnt(0)
	v_add_f32_e32 v251, v251, v13
	v_fmamk_f32 v251, v251, 0x3a800000, v224
	v_rsq_f32_e32 v244, v244
	v_rsq_f32_e32 v245, v245
	v_rsq_f32_e32 v246, v246
	v_rsq_f32_e32 v247, v247
	v_rsq_f32_e32 v248, v248
	v_rsq_f32_e32 v249, v249
	v_rsq_f32_e32 v250, v250
	v_rsq_f32_e32 v251, v251
	v_pk_mul_f32 v[6:7], v[158:159], v[244:245] op_sel_hi:[1,0]
	v_pk_mul_f32 v[8:9], v[160:161], v[244:245] op_sel_hi:[1,0]
	v_pk_mul_f32 v[10:11], v[150:151], v[244:245] op_sel_hi:[1,0]
	v_pk_mul_f32 v[12:13], v[6:7], v[2:3] op_sel_hi:[1,0]
	v_pk_mul_f32 v[14:15], v[8:9], v[2:3] op_sel_hi:[1,0]
	v_pk_mul_f32 v[16:17], v[10:11], v[2:3] op_sel_hi:[1,0]
	v_exp_f32_e32 v12, v12
	v_pk_mul_f32 v[18:19], v[152:153], v[244:245] op_sel_hi:[1,0]
	v_exp_f32_e32 v14, v14
	v_pk_mul_f32 v[20:21], v[142:143], v[244:245] op_sel:[0,1] op_sel_hi:[1,1]
	v_exp_f32_e32 v16, v16
	v_pk_mul_f32 v[22:23], v[18:19], v[2:3] op_sel_hi:[1,0]
	v_pk_mul_f32 v[24:25], v[20:21], v[2:3] op_sel_hi:[1,0]
	v_pk_mul_f32 v[26:27], v[144:145], v[244:245] op_sel:[0,1] op_sel_hi:[1,1]
	v_exp_f32_e32 v22, v22
	v_pk_mul_f32 v[28:29], v[134:135], v[244:245] op_sel:[0,1] op_sel_hi:[1,1]
	v_exp_f32_e32 v13, v13
	v_pk_mul_f32 v[30:31], v[26:27], v[2:3] op_sel_hi:[1,0]
	v_exp_f32_e32 v15, v15
	v_pk_mul_f32 v[32:33], v[28:29], v[2:3] op_sel_hi:[1,0]
	v_exp_f32_e32 v17, v17
	v_pk_mul_f32 v[186:187], v[136:137], v[244:245] op_sel:[0,1] op_sel_hi:[1,1]
	v_exp_f32_e32 v23, v23
	v_pk_mul_f32 v[188:189], v[154:155], v[244:245] op_sel_hi:[1,0]
	v_pk_fma_f32 v[12:13], v[12:13], v[2:3], v[2:3] op_sel:[0,1,1] op_sel_hi:[1,1,1]
	v_exp_f32_e32 v24, v24
	v_pk_fma_f32 v[14:15], v[14:15], v[2:3], v[2:3] op_sel:[0,1,1] op_sel_hi:[1,1,1]
	v_rcp_f32_e32 v12, v12
	v_pk_fma_f32 v[16:17], v[16:17], v[2:3], v[2:3] op_sel:[0,1,1] op_sel_hi:[1,1,1]
	v_rcp_f32_e32 v14, v14
	v_pk_fma_f32 v[22:23], v[22:23], v[2:3], v[2:3] op_sel:[0,1,1] op_sel_hi:[1,1,1]
	v_rcp_f32_e32 v16, v16
	v_pk_mul_f32 v[190:191], v[186:187], v[2:3] op_sel_hi:[1,0]
	v_rcp_f32_e32 v22, v22
	v_pk_mul_f32 v[188:189], v[188:189], v[6:7]
	v_exp_f32_e32 v30, v30
	v_pk_mul_f32 v[6:7], v[156:157], v[244:245] op_sel_hi:[1,0]
	v_exp_f32_e32 v32, v32
	v_pk_mul_f32 v[192:193], v[146:147], v[244:245] op_sel_hi:[1,0]
	v_rcp_f32_e32 v13, v13
	v_pk_mul_f32 v[200:201], v[126:127], v[246:247] op_sel_hi:[1,0]
	v_exp_f32_e32 v190, v190
	v_pk_mul_f32 v[6:7], v[6:7], v[8:9]
	v_rcp_f32_e32 v15, v15
	v_pk_mul_f32 v[192:193], v[192:193], v[10:11]
	v_rcp_f32_e32 v17, v17
	v_pk_mul_f32 v[8:9], v[148:149], v[244:245] op_sel_hi:[1,0]
	v_exp_f32_e32 v25, v25
	v_pk_mul_f32 v[188:189], v[188:189], v[12:13]
	v_rcp_f32_e32 v23, v23
	v_pk_mul_f32 v[10:11], v[200:201], v[2:3] op_sel_hi:[1,0]
	v_exp_f32_e32 v31, v31
	v_med3_f32 v188, v188, s87, v227
	v_exp_f32_e32 v33, v33
	v_pk_mul_f32 v[6:7], v[6:7], v[14:15]
	v_exp_f32_e32 v191, v191
	v_pk_mul_f32 v[192:193], v[192:193], v[16:17]
	v_pk_fma_f32 v[24:25], v[24:25], v[2:3], v[2:3] op_sel:[0,1,1] op_sel_hi:[1,1,1]
	v_med3_f32 v189, v189, s87, v227
	v_med3_f32 v6, v6, s87, v227
	v_med3_f32 v192, v192, s87, v227
	v_rcp_f32_e32 v24, v24
	v_pk_fma_f32 v[30:31], v[30:31], v[2:3], v[2:3] op_sel:[0,1,1] op_sel_hi:[1,1,1]
	v_pk_fma_f32 v[32:33], v[32:33], v[2:3], v[2:3] op_sel:[0,1,1] op_sel_hi:[1,1,1]
	v_pk_mul_f32 v[12:13], v[128:129], v[246:247] op_sel_hi:[1,0]
	v_pk_mul_f32 v[14:15], v[118:119], v[246:247] op_sel_hi:[1,0]
	v_cvt_pk_fp8_f32 v16, v188, v189
	v_med3_f32 v7, v7, s87, v227
	v_med3_f32 v193, v193, s87, v227
	v_pk_mul_f32 v[8:9], v[8:9], v[18:19]
	v_rcp_f32_e32 v30, v30
	v_pk_fma_f32 v[190:191], v[190:191], v[2:3], v[2:3] op_sel:[0,1,1] op_sel_hi:[1,1,1]
	v_pk_mul_f32 v[8:9], v[8:9], v[22:23]
	v_rcp_f32_e32 v32, v32
	v_pk_mul_f32 v[18:19], v[12:13], v[2:3] op_sel_hi:[1,0]
	v_med3_f32 v8, v8, s87, v227
	v_exp_f32_e32 v10, v10
	v_pk_mul_f32 v[22:23], v[14:15], v[2:3] op_sel_hi:[1,0]
	v_pk_mul_f32 v[188:189], v[120:121], v[246:247] op_sel_hi:[1,0]
	v_cvt_pk_fp8_f32 v16, v6, v7 op_sel:[0,0,1]
	v_cvt_pk_fp8_f32 v17, v192, v193
	v_med3_f32 v9, v9, s87, v227
	v_rcp_f32_e32 v190, v190
	v_pk_mul_f32 v[6:7], v[188:189], v[2:3] op_sel_hi:[1,0]
	v_exp_f32_e32 v18, v18
	v_cvt_pk_fp8_f32 v17, v8, v9 op_sel:[0,0,1]
	v_exp_f32_e32 v22, v22
	v_pk_mul_f32 v[8:9], v[138:139], v[244:245] op_sel:[0,1] op_sel_hi:[1,1]
	v_rcp_f32_e32 v25, v25
	global_store_dwordx2 v241, v[16:17], s[26:27]
	v_exp_f32_e32 v6, v6
	v_pk_mul_f32 v[8:9], v[8:9], v[20:21]
	v_rcp_f32_e32 v31, v31
	v_pk_mul_f32 v[16:17], v[140:141], v[244:245] op_sel:[0,1] op_sel_hi:[1,1]
	v_rcp_f32_e32 v33, v33
	v_pk_mul_f32 v[20:21], v[130:131], v[244:245] op_sel:[0,1] op_sel_hi:[1,1]
	v_exp_f32_e32 v11, v11
	v_pk_mul_f32 v[8:9], v[8:9], v[24:25]
	v_rcp_f32_e32 v191, v191
	v_pk_mul_f32 v[24:25], v[110:111], v[246:247] op_sel:[0,1] op_sel_hi:[1,1]
	v_exp_f32_e32 v19, v19
	v_med3_f32 v8, v8, s87, v227
	v_exp_f32_e32 v23, v23
	v_pk_mul_f32 v[16:17], v[16:17], v[26:27]
	v_exp_f32_e32 v7, v7
	v_pk_fma_f32 v[10:11], v[10:11], v[2:3], v[2:3] op_sel:[0,1,1] op_sel_hi:[1,1,1]
	v_pk_mul_f32 v[16:17], v[16:17], v[30:31]
	v_med3_f32 v9, v9, s87, v227
	v_pk_mul_f32 v[20:21], v[20:21], v[28:29]
	v_med3_f32 v16, v16, s87, v227
	v_pk_mul_f32 v[26:27], v[132:133], v[244:245] op_sel:[0,1] op_sel_hi:[1,1]
	v_pk_mul_f32 v[20:21], v[20:21], v[32:33]
	v_rcp_f32_e32 v10, v10
	v_pk_fma_f32 v[18:19], v[18:19], v[2:3], v[2:3] op_sel:[0,1,1] op_sel_hi:[1,1,1]
	v_med3_f32 v20, v20, s87, v227
	v_pk_fma_f32 v[22:23], v[22:23], v[2:3], v[2:3] op_sel:[0,1,1] op_sel_hi:[1,1,1]
	v_pk_mul_f32 v[28:29], v[24:25], v[2:3] op_sel_hi:[1,0]
	v_pk_mul_f32 v[30:31], v[112:113], v[246:247] op_sel:[0,1] op_sel_hi:[1,1]
	v_pk_mul_f32 v[32:33], v[102:103], v[246:247] op_sel:[0,1] op_sel_hi:[1,1]
	v_cvt_pk_fp8_f32 v8, v8, v9
	v_med3_f32 v17, v17, s87, v227
	v_med3_f32 v21, v21, s87, v227
	v_pk_mul_f32 v[26:27], v[26:27], v[186:187]
	v_rcp_f32_e32 v18, v18
	v_pk_fma_f32 v[6:7], v[6:7], v[2:3], v[2:3] op_sel:[0,1,1] op_sel_hi:[1,1,1]
	v_pk_mul_f32 v[26:27], v[26:27], v[190:191]
	v_rcp_f32_e32 v22, v22
	v_pk_mul_f32 v[186:187], v[30:31], v[2:3] op_sel_hi:[1,0]
	v_med3_f32 v26, v26, s87, v227
	v_exp_f32_e32 v28, v28
	v_pk_mul_f32 v[190:191], v[32:33], v[2:3] op_sel_hi:[1,0]
	v_pk_mul_f32 v[192:193], v[104:105], v[246:247] op_sel:[0,1] op_sel_hi:[1,1]
	v_cvt_pk_fp8_f32 v8, v16, v17 op_sel:[0,0,1]
	v_cvt_pk_fp8_f32 v9, v20, v21
	v_med3_f32 v27, v27, s87, v227
	v_rcp_f32_e32 v6, v6
	v_pk_mul_f32 v[16:17], v[192:193], v[2:3] op_sel_hi:[1,0]
	v_exp_f32_e32 v186, v186
	v_cvt_pk_fp8_f32 v9, v26, v27 op_sel:[0,0,1]
	v_exp_f32_e32 v190, v190
	v_pk_mul_f32 v[20:21], v[122:123], v[246:247] op_sel_hi:[1,0]
	v_rcp_f32_e32 v11, v11
	v_pk_mul_f32 v[26:27], v[124:125], v[246:247] op_sel_hi:[1,0]
	v_exp_f32_e32 v16, v16
	v_pk_mul_f32 v[20:21], v[20:21], v[200:201]
	v_rcp_f32_e32 v19, v19
	v_pk_mul_f32 v[200:201], v[114:115], v[246:247] op_sel_hi:[1,0]
	v_rcp_f32_e32 v23, v23
	v_pk_mul_f32 v[202:203], v[94:95], v[248:249] op_sel_hi:[1,0]
	v_exp_f32_e32 v29, v29
	v_pk_mul_f32 v[20:21], v[20:21], v[10:11]
	v_rcp_f32_e32 v7, v7
	v_pk_mul_f32 v[26:27], v[26:27], v[12:13]
	v_exp_f32_e32 v187, v187
	v_med3_f32 v20, v20, s87, v227
	v_exp_f32_e32 v191, v191
	v_pk_mul_f32 v[26:27], v[26:27], v[18:19]
	v_exp_f32_e32 v17, v17
	v_pk_fma_f32 v[28:29], v[28:29], v[2:3], v[2:3] op_sel:[0,1,1] op_sel_hi:[1,1,1]
	v_med3_f32 v21, v21, s87, v227
	v_med3_f32 v26, v26, s87, v227
	v_pk_mul_f32 v[200:201], v[200:201], v[14:15]
	v_pk_mul_f32 v[10:11], v[116:117], v[246:247] op_sel_hi:[1,0]
	v_rcp_f32_e32 v28, v28
	v_pk_mul_f32 v[200:201], v[200:201], v[22:23]
	v_pk_fma_f32 v[186:187], v[186:187], v[2:3], v[2:3] op_sel:[0,1,1] op_sel_hi:[1,1,1]
	v_pk_fma_f32 v[190:191], v[190:191], v[2:3], v[2:3] op_sel:[0,1,1] op_sel_hi:[1,1,1]
	v_med3_f32 v200, v200, s87, v227
	v_pk_mul_f32 v[12:13], v[202:203], v[2:3] op_sel_hi:[1,0]
	v_pk_mul_f32 v[14:15], v[96:97], v[248:249] op_sel_hi:[1,0]
	v_pk_mul_f32 v[18:19], v[86:87], v[248:249] op_sel_hi:[1,0]
	v_cvt_pk_fp8_f32 v20, v20, v21
	v_med3_f32 v27, v27, s87, v227
	v_med3_f32 v201, v201, s87, v227
	v_pk_mul_f32 v[10:11], v[10:11], v[188:189]
	v_rcp_f32_e32 v186, v186
	v_pk_fma_f32 v[16:17], v[16:17], v[2:3], v[2:3] op_sel:[0,1,1] op_sel_hi:[1,1,1]
	v_pk_mul_f32 v[10:11], v[10:11], v[6:7]
	v_rcp_f32_e32 v190, v190
	v_pk_mul_f32 v[6:7], v[14:15], v[2:3] op_sel_hi:[1,0]
	v_med3_f32 v10, v10, s87, v227
	v_exp_f32_e32 v12, v12
	v_pk_mul_f32 v[22:23], v[18:19], v[2:3] op_sel_hi:[1,0]
	v_pk_mul_f32 v[188:189], v[88:89], v[248:249] op_sel_hi:[1,0]
	v_cvt_pk_fp8_f32 v20, v26, v27 op_sel:[0,0,1]
	v_cvt_pk_fp8_f32 v21, v200, v201
	v_med3_f32 v11, v11, s87, v227
	v_rcp_f32_e32 v16, v16
	v_pk_mul_f32 v[26:27], v[188:189], v[2:3] op_sel_hi:[1,0]
	v_exp_f32_e32 v6, v6
	v_add_u32_e32 v200, 0xe000, v241
	v_exp_f32_e32 v22, v22
	v_cvt_pk_fp8_f32 v21, v10, v11 op_sel:[0,0,1]
	global_store_dwordx2 v200, v[8:9], s[26:27]
	v_rcp_f32_e32 v29, v29
	v_pk_mul_f32 v[8:9], v[106:107], v[246:247] op_sel:[0,1] op_sel_hi:[1,1]
	v_exp_f32_e32 v26, v26
	v_pk_mul_f32 v[10:11], v[108:109], v[246:247] op_sel:[0,1] op_sel_hi:[1,1]
	v_rcp_f32_e32 v187, v187
	v_pk_mul_f32 v[8:9], v[8:9], v[24:25]
	v_rcp_f32_e32 v191, v191
	v_pk_mul_f32 v[24:25], v[98:99], v[246:247] op_sel:[0,1] op_sel_hi:[1,1]
	v_exp_f32_e32 v13, v13
	v_pk_mul_f32 v[8:9], v[8:9], v[28:29]
	v_rcp_f32_e32 v17, v17
	v_pk_mul_f32 v[28:29], v[78:79], v[248:249] op_sel:[0,1] op_sel_hi:[1,1]
	v_exp_f32_e32 v7, v7
	v_med3_f32 v8, v8, s87, v227
	v_exp_f32_e32 v23, v23
	v_pk_mul_f32 v[10:11], v[10:11], v[30:31]
	v_exp_f32_e32 v27, v27
	v_pk_fma_f32 v[12:13], v[12:13], v[2:3], v[2:3] op_sel:[0,1,1] op_sel_hi:[1,1,1]
	v_pk_mul_f32 v[10:11], v[10:11], v[186:187]
	v_med3_f32 v9, v9, s87, v227
	v_pk_mul_f32 v[24:25], v[24:25], v[32:33]
	v_med3_f32 v10, v10, s87, v227
	v_pk_mul_f32 v[30:31], v[100:101], v[246:247] op_sel:[0,1] op_sel_hi:[1,1]
	v_pk_mul_f32 v[24:25], v[24:25], v[190:191]
	v_rcp_f32_e32 v12, v12
	v_pk_fma_f32 v[6:7], v[6:7], v[2:3], v[2:3] op_sel:[0,1,1] op_sel_hi:[1,1,1]
	v_med3_f32 v24, v24, s87, v227
	v_pk_fma_f32 v[22:23], v[22:23], v[2:3], v[2:3] op_sel:[0,1,1] op_sel_hi:[1,1,1]
	v_pk_mul_f32 v[32:33], v[28:29], v[2:3] op_sel_hi:[1,0]
	v_pk_mul_f32 v[186:187], v[80:81], v[248:249] op_sel:[0,1] op_sel_hi:[1,1]
	v_pk_mul_f32 v[190:191], v[70:71], v[248:249] op_sel:[0,1] op_sel_hi:[1,1]
	v_cvt_pk_fp8_f32 v8, v8, v9
	v_med3_f32 v11, v11, s87, v227
	v_med3_f32 v25, v25, s87, v227
	v_pk_mul_f32 v[30:31], v[30:31], v[192:193]
	v_rcp_f32_e32 v6, v6
	v_pk_fma_f32 v[26:27], v[26:27], v[2:3], v[2:3] op_sel:[0,1,1] op_sel_hi:[1,1,1]
	v_pk_mul_f32 v[30:31], v[30:31], v[16:17]
	v_rcp_f32_e32 v22, v22
	v_pk_mul_f32 v[16:17], v[186:187], v[2:3] op_sel_hi:[1,0]
	v_med3_f32 v30, v30, s87, v227
	v_exp_f32_e32 v32, v32
	v_pk_mul_f32 v[192:193], v[190:191], v[2:3] op_sel_hi:[1,0]
	v_pk_mul_f32 v[200:201], v[72:73], v[248:249] op_sel:[0,1] op_sel_hi:[1,1]
	v_cvt_pk_fp8_f32 v8, v10, v11 op_sel:[0,0,1]
	v_cvt_pk_fp8_f32 v9, v24, v25
	v_med3_f32 v31, v31, s87, v227
	v_rcp_f32_e32 v26, v26
	v_pk_mul_f32 v[10:11], v[200:201], v[2:3] op_sel_hi:[1,0]
	v_exp_f32_e32 v16, v16
	v_add_u32_e32 v24, 0x1c000, v241
	v_exp_f32_e32 v192, v192
	v_cvt_pk_fp8_f32 v9, v30, v31 op_sel:[0,0,1]
	global_store_dwordx2 v24, v[20:21], s[26:27]
	v_rcp_f32_e32 v13, v13
	v_pk_mul_f32 v[20:21], v[90:91], v[248:249] op_sel_hi:[1,0]
	v_exp_f32_e32 v10, v10
	v_pk_mul_f32 v[24:25], v[92:93], v[248:249] op_sel_hi:[1,0]
	v_rcp_f32_e32 v7, v7
	v_pk_mul_f32 v[20:21], v[20:21], v[202:203]
	v_rcp_f32_e32 v23, v23
	v_pk_mul_f32 v[30:31], v[82:83], v[248:249] op_sel_hi:[1,0]
	v_exp_f32_e32 v33, v33
	v_pk_mul_f32 v[20:21], v[20:21], v[12:13]
	v_rcp_f32_e32 v27, v27
	v_pk_mul_f32 v[12:13], v[62:63], v[250:251] op_sel_hi:[1,0]
	v_exp_f32_e32 v17, v17
	v_med3_f32 v20, v20, s87, v227
	v_exp_f32_e32 v193, v193
	v_pk_mul_f32 v[24:25], v[24:25], v[14:15]
	v_exp_f32_e32 v11, v11
	v_pk_fma_f32 v[32:33], v[32:33], v[2:3], v[2:3] op_sel:[0,1,1] op_sel_hi:[1,1,1]
	v_pk_mul_f32 v[24:25], v[24:25], v[6:7]
	v_med3_f32 v21, v21, s87, v227
	v_pk_mul_f32 v[30:31], v[30:31], v[18:19]
	v_med3_f32 v24, v24, s87, v227
	v_pk_mul_f32 v[6:7], v[84:85], v[248:249] op_sel_hi:[1,0]
	v_pk_mul_f32 v[30:31], v[30:31], v[22:23]
	v_rcp_f32_e32 v32, v32
	v_pk_fma_f32 v[16:17], v[16:17], v[2:3], v[2:3] op_sel:[0,1,1] op_sel_hi:[1,1,1]
	v_med3_f32 v30, v30, s87, v227
	v_pk_fma_f32 v[192:193], v[192:193], v[2:3], v[2:3] op_sel:[0,1,1] op_sel_hi:[1,1,1]
	v_pk_mul_f32 v[14:15], v[12:13], v[2:3] op_sel_hi:[1,0]
	v_pk_mul_f32 v[18:19], v[64:65], v[250:251] op_sel_hi:[1,0]
	v_pk_mul_f32 v[22:23], v[54:55], v[250:251] op_sel_hi:[1,0]
	v_cvt_pk_fp8_f32 v20, v20, v21
	v_med3_f32 v25, v25, s87, v227
	v_med3_f32 v31, v31, s87, v227
	v_pk_mul_f32 v[6:7], v[6:7], v[188:189]
	v_rcp_f32_e32 v16, v16
	v_pk_fma_f32 v[10:11], v[10:11], v[2:3], v[2:3] op_sel:[0,1,1] op_sel_hi:[1,1,1]
	v_pk_mul_f32 v[6:7], v[6:7], v[26:27]
	v_rcp_f32_e32 v192, v192
	v_pk_mul_f32 v[26:27], v[18:19], v[2:3] op_sel_hi:[1,0]
	v_med3_f32 v6, v6, s87, v227
	v_exp_f32_e32 v14, v14
	v_pk_mul_f32 v[188:189], v[22:23], v[2:3] op_sel_hi:[1,0]
	v_pk_mul_f32 v[202:203], v[56:57], v[250:251] op_sel_hi:[1,0]
	v_cvt_pk_fp8_f32 v20, v24, v25 op_sel:[0,0,1]
	v_cvt_pk_fp8_f32 v21, v30, v31
	v_med3_f32 v7, v7, s87, v227
	v_rcp_f32_e32 v10, v10
	v_pk_mul_f32 v[24:25], v[202:203], v[2:3] op_sel_hi:[1,0]
	v_exp_f32_e32 v26, v26
	v_add_u32_e32 v30, 0x2a000, v241
	v_exp_f32_e32 v188, v188
	v_cvt_pk_fp8_f32 v21, v6, v7 op_sel:[0,0,1]
	global_store_dwordx2 v30, v[8:9], s[26:27]
	v_rcp_f32_e32 v33, v33
	v_pk_mul_f32 v[6:7], v[74:75], v[248:249] op_sel:[0,1] op_sel_hi:[1,1]
	v_exp_f32_e32 v24, v24
	v_pk_mul_f32 v[8:9], v[76:77], v[248:249] op_sel:[0,1] op_sel_hi:[1,1]
	v_rcp_f32_e32 v17, v17
	v_pk_mul_f32 v[6:7], v[6:7], v[28:29]
	v_rcp_f32_e32 v193, v193
	v_pk_mul_f32 v[28:29], v[66:67], v[248:249] op_sel:[0,1] op_sel_hi:[1,1]
	v_exp_f32_e32 v15, v15
	v_pk_mul_f32 v[6:7], v[6:7], v[32:33]
	v_rcp_f32_e32 v11, v11
	v_pk_mul_f32 v[30:31], v[46:47], v[250:251] op_sel:[0,1] op_sel_hi:[1,1]
	v_exp_f32_e32 v27, v27
	v_med3_f32 v6, v6, s87, v227
	v_exp_f32_e32 v189, v189
	v_pk_mul_f32 v[8:9], v[8:9], v[186:187]
	v_exp_f32_e32 v25, v25
	v_pk_fma_f32 v[14:15], v[14:15], v[2:3], v[2:3] op_sel:[0,1,1] op_sel_hi:[1,1,1]
	v_pk_mul_f32 v[8:9], v[8:9], v[16:17]
	v_med3_f32 v7, v7, s87, v227
	v_pk_mul_f32 v[28:29], v[28:29], v[190:191]
	v_med3_f32 v8, v8, s87, v227
	v_pk_mul_f32 v[16:17], v[68:69], v[248:249] op_sel:[0,1] op_sel_hi:[1,1]
	v_pk_mul_f32 v[28:29], v[28:29], v[192:193]
	v_rcp_f32_e32 v14, v14
	v_pk_fma_f32 v[26:27], v[26:27], v[2:3], v[2:3] op_sel:[0,1,1] op_sel_hi:[1,1,1]
	v_med3_f32 v28, v28, s87, v227
	v_pk_fma_f32 v[188:189], v[188:189], v[2:3], v[2:3] op_sel:[0,1,1] op_sel_hi:[1,1,1]
	v_pk_mul_f32 v[32:33], v[30:31], v[2:3] op_sel_hi:[1,0]
	v_pk_mul_f32 v[186:187], v[48:49], v[250:251] op_sel:[0,1] op_sel_hi:[1,1]
	v_pk_mul_f32 v[190:191], v[38:39], v[250:251] op_sel:[0,1] op_sel_hi:[1,1]
	v_cvt_pk_fp8_f32 v6, v6, v7
	v_med3_f32 v9, v9, s87, v227
	v_med3_f32 v29, v29, s87, v227
	v_pk_mul_f32 v[16:17], v[16:17], v[200:201]
	v_rcp_f32_e32 v26, v26
	v_pk_fma_f32 v[24:25], v[24:25], v[2:3], v[2:3] op_sel:[0,1,1] op_sel_hi:[1,1,1]
	v_pk_mul_f32 v[16:17], v[16:17], v[10:11]
	v_rcp_f32_e32 v188, v188
	v_pk_mul_f32 v[10:11], v[186:187], v[2:3] op_sel_hi:[1,0]
	v_med3_f32 v16, v16, s87, v227
	v_exp_f32_e32 v32, v32
	v_pk_mul_f32 v[192:193], v[190:191], v[2:3] op_sel_hi:[1,0]
	v_pk_mul_f32 v[200:201], v[40:41], v[250:251] op_sel:[0,1] op_sel_hi:[1,1]
	v_cvt_pk_fp8_f32 v6, v8, v9 op_sel:[0,0,1]
	v_cvt_pk_fp8_f32 v7, v28, v29
	v_med3_f32 v17, v17, s87, v227
	v_rcp_f32_e32 v24, v24
	v_pk_mul_f32 v[8:9], v[200:201], v[2:3] op_sel_hi:[1,0]
	v_exp_f32_e32 v10, v10
	v_add_u32_e32 v28, 0x70000, v241
	v_exp_f32_e32 v192, v192
	v_cvt_pk_fp8_f32 v7, v16, v17 op_sel:[0,0,1]
	global_store_dwordx2 v28, v[20:21], s[26:27]
	v_rcp_f32_e32 v15, v15
	v_pk_mul_f32 v[16:17], v[58:59], v[250:251] op_sel_hi:[1,0]
	v_exp_f32_e32 v8, v8
	v_pk_mul_f32 v[20:21], v[60:61], v[250:251] op_sel_hi:[1,0]
	v_rcp_f32_e32 v27, v27
	v_pk_mul_f32 v[16:17], v[16:17], v[12:13]
	v_rcp_f32_e32 v189, v189
	v_pk_mul_f32 v[12:13], v[50:51], v[250:251] op_sel_hi:[1,0]
	v_exp_f32_e32 v33, v33
	v_pk_mul_f32 v[16:17], v[16:17], v[14:15]
	v_rcp_f32_e32 v25, v25
	v_pk_mul_f32 v[20:21], v[20:21], v[18:19]
	v_exp_f32_e32 v11, v11
	v_med3_f32 v16, v16, s87, v227
	v_exp_f32_e32 v193, v193
	v_pk_mul_f32 v[20:21], v[20:21], v[26:27]
	v_exp_f32_e32 v9, v9
	v_pk_fma_f32 v[32:33], v[32:33], v[2:3], v[2:3] op_sel:[0,1,1] op_sel_hi:[1,1,1]
	v_med3_f32 v17, v17, s87, v227
	v_med3_f32 v20, v20, s87, v227
	v_pk_mul_f32 v[12:13], v[12:13], v[22:23]
	v_pk_mul_f32 v[14:15], v[52:53], v[250:251] op_sel_hi:[1,0]
	v_rcp_f32_e32 v32, v32
	v_pk_mul_f32 v[12:13], v[12:13], v[188:189]
	v_pk_fma_f32 v[10:11], v[10:11], v[2:3], v[2:3] op_sel:[0,1,1] op_sel_hi:[1,1,1]
	v_pk_fma_f32 v[192:193], v[192:193], v[2:3], v[2:3] op_sel:[0,1,1] op_sel_hi:[1,1,1]
	v_med3_f32 v12, v12, s87, v227
	v_cvt_pk_fp8_f32 v16, v16, v17
	v_med3_f32 v21, v21, s87, v227
	v_med3_f32 v13, v13, s87, v227
	v_pk_mul_f32 v[14:15], v[14:15], v[202:203]
	v_rcp_f32_e32 v10, v10
	v_pk_fma_f32 v[8:9], v[8:9], v[2:3], v[2:3] op_sel:[0,1,1] op_sel_hi:[1,1,1]
	v_pk_mul_f32 v[14:15], v[14:15], v[24:25]
	v_rcp_f32_e32 v192, v192
	v_cvt_pk_fp8_f32 v16, v20, v21 op_sel:[0,0,1]
	v_med3_f32 v14, v14, s87, v227
	v_cvt_pk_fp8_f32 v17, v12, v13
	v_rcp_f32_e32 v8, v8
	v_med3_f32 v15, v15, s87, v227
	v_add_u32_e32 v12, 0x7e000, v241
	v_rcp_f32_e32 v33, v33
	v_cvt_pk_fp8_f32 v17, v14, v15 op_sel:[0,0,1]
	global_store_dwordx2 v12, v[6:7], s[26:27]
	v_rcp_f32_e32 v11, v11
	v_pk_mul_f32 v[6:7], v[42:43], v[250:251] op_sel:[0,1] op_sel_hi:[1,1]
	v_rcp_f32_e32 v193, v193
	v_pk_mul_f32 v[12:13], v[44:45], v[250:251] op_sel:[0,1] op_sel_hi:[1,1]
	v_rcp_f32_e32 v9, v9
	v_pk_mul_f32 v[6:7], v[6:7], v[30:31]
	v_pk_mul_f32 v[14:15], v[34:35], v[250:251] op_sel:[0,1] op_sel_hi:[1,1]
	v_pk_mul_f32 v[12:13], v[12:13], v[186:187]
	v_pk_mul_f32 v[6:7], v[6:7], v[32:33]
	v_pk_mul_f32 v[14:15], v[14:15], v[190:191]
	v_pk_mul_f32 v[12:13], v[12:13], v[10:11]
	v_med3_f32 v6, v6, s87, v227
	v_pk_mul_f32 v[14:15], v[14:15], v[192:193]
	v_med3_f32 v12, v12, s87, v227
	v_med3_f32 v7, v7, s87, v227
	v_med3_f32 v14, v14, s87, v227
	v_pk_mul_f32 v[10:11], v[36:37], v[250:251] op_sel:[0,1] op_sel_hi:[1,1]
	v_cvt_pk_fp8_f32 v6, v6, v7
	v_med3_f32 v13, v13, s87, v227
	v_med3_f32 v15, v15, s87, v227
	v_pk_mul_f32 v[10:11], v[10:11], v[200:201]
	v_cvt_pk_fp8_f32 v6, v12, v13 op_sel:[0,0,1]
	v_cvt_pk_fp8_f32 v7, v14, v15
	v_pk_mul_f32 v[10:11], v[10:11], v[8:9]
	v_add_u32_e32 v8, 0x8c000, v241
	v_add_u32_e32 v9, 0x9a000, v241
	v_med3_f32 v10, v10, s87, v227
	global_store_dwordx2 v8, v[16:17], s[26:27]
	v_med3_f32 v11, v11, s87, v227
	v_cvt_pk_fp8_f32 v7, v10, v11 op_sel:[0,0,1]
	global_store_dwordx2 v9, v[6:7], s[26:27]
	s_andn2_b64 vcc, exec, s[44:45]
	s_mov_b64 s[44:45], -1
	s_cbranch_vccnz .LBB0_832
	s_andn2_b64 vcc, exec, s[30:31]
	s_cbranch_vccnz .LBB0_831
	s_barrier
	s_branch .LBB0_831

.LBB0_1697:
	v_mov_b32_e32 v2, 0xbfb8aa3b
	v_mov_b32_e32 v3, 0x3e000000
	v_mov_b32_e32 v4, 0x41000000
	v_lshl_add_u32 v251, s60, 8, v209
	v_lshl_or_b32 v250, s58, 7, v211
	v_mad_u32_u24 v249, v251, s33, v250
	v_pk_mul_f32 v[6:7], v[154:155], v[2:3] op_sel_hi:[1,0]
	v_pk_mul_f32 v[8:9], v[156:157], v[2:3] op_sel_hi:[1,0]
	v_pk_mul_f32 v[10:11], v[150:151], v[2:3] op_sel_hi:[1,0]
	v_exp_f32_e32 v6, v6
	v_pk_mul_f32 v[12:13], v[152:153], v[2:3] op_sel_hi:[1,0]
	v_exp_f32_e32 v8, v8
	v_pk_mul_f32 v[14:15], v[142:143], v[2:3] op_sel_hi:[1,0]
	v_exp_f32_e32 v10, v10
	v_pk_mul_f32 v[16:17], v[144:145], v[2:3] op_sel_hi:[1,0]
	v_exp_f32_e32 v12, v12
	v_pk_mul_f32 v[18:19], v[134:135], v[2:3] op_sel_hi:[1,0]
	v_exp_f32_e32 v7, v7
	v_pk_mul_f32 v[20:21], v[136:137], v[2:3] op_sel_hi:[1,0]
	v_exp_f32_e32 v9, v9
	v_pk_mul_f32 v[22:23], v[126:127], v[2:3] op_sel_hi:[1,0]
	v_exp_f32_e32 v11, v11
	v_pk_mul_f32 v[24:25], v[128:129], v[2:3] op_sel_hi:[1,0]
	v_exp_f32_e32 v13, v13
	v_pk_mul_f32 v[26:27], v[118:119], v[2:3] op_sel_hi:[1,0]
	v_exp_f32_e32 v14, v14
	v_pk_fma_f32 v[6:7], v[6:7], v[2:3], v[2:3] op_sel:[0,1,1] op_sel_hi:[1,1,1]
	v_exp_f32_e32 v16, v16
	v_pk_fma_f32 v[8:9], v[8:9], v[2:3], v[2:3] op_sel:[0,1,1] op_sel_hi:[1,1,1]
	v_exp_f32_e32 v18, v18
	v_pk_fma_f32 v[10:11], v[10:11], v[2:3], v[2:3] op_sel:[0,1,1] op_sel_hi:[1,1,1]
	v_rcp_f32_e32 v6, v6
	v_pk_fma_f32 v[12:13], v[12:13], v[2:3], v[2:3] op_sel:[0,1,1] op_sel_hi:[1,1,1]
	v_exp_f32_e32 v20, v20
	v_pk_mul_f32 v[28:29], v[120:121], v[2:3] op_sel_hi:[1,0]
	v_rcp_f32_e32 v8, v8
	v_pk_mul_f32 v[30:31], v[154:155], v[158:159]
	v_rcp_f32_e32 v10, v10
	v_pk_mul_f32 v[32:33], v[110:111], v[2:3] op_sel_hi:[1,0]
	v_exp_f32_e32 v15, v15
	v_pk_mul_f32 v[196:197], v[156:157], v[160:161]
	v_rcp_f32_e32 v12, v12
	v_pk_mul_f32 v[198:199], v[150:151], v[146:147]
	v_exp_f32_e32 v17, v17
	v_pk_mul_f32 v[200:201], v[112:113], v[2:3] op_sel_hi:[1,0]
	v_exp_f32_e32 v19, v19
	v_pk_mul_f32 v[202:203], v[102:103], v[2:3] op_sel_hi:[1,0]
	v_rcp_f32_e32 v7, v7
	v_pk_fma_f32 v[14:15], v[14:15], v[2:3], v[2:3] op_sel:[0,1,1] op_sel_hi:[1,1,1]
	v_exp_f32_e32 v21, v21
	v_pk_mul_f32 v[214:215], v[152:153], v[148:149]
	v_exp_f32_e32 v22, v22
	v_pk_fma_f32 v[16:17], v[16:17], v[2:3], v[2:3] op_sel:[0,1,1] op_sel_hi:[1,1,1]
	v_rcp_f32_e32 v9, v9
	v_pk_fma_f32 v[18:19], v[18:19], v[2:3], v[2:3] op_sel:[0,1,1] op_sel_hi:[1,1,1]
	v_rcp_f32_e32 v11, v11
	v_pk_mul_f32 v[30:31], v[30:31], v[6:7]
	v_exp_f32_e32 v24, v24
	v_pk_fma_f32 v[20:21], v[20:21], v[2:3], v[2:3] op_sel:[0,1,1] op_sel_hi:[1,1,1]
	v_exp_f32_e32 v26, v26
	v_med3_f32 v30, v30, s87, v227
	v_rcp_f32_e32 v13, v13
	v_pk_mul_f32 v[196:197], v[196:197], v[8:9]
	v_rcp_f32_e32 v14, v14
	v_pk_mul_f32 v[198:199], v[198:199], v[10:11]
	v_exp_f32_e32 v28, v28
	v_med3_f32 v31, v31, s87, v227
	v_rcp_f32_e32 v16, v16
	v_med3_f32 v196, v196, s87, v227
	v_rcp_f32_e32 v18, v18
	v_med3_f32 v198, v198, s87, v227
	v_exp_f32_e32 v23, v23
	v_pk_mul_f32 v[214:215], v[214:215], v[12:13]
	v_rcp_f32_e32 v20, v20
	v_cvt_pk_fp8_f32 v6, v30, v31
	v_exp_f32_e32 v25, v25
	v_med3_f32 v197, v197, s87, v227
	v_exp_f32_e32 v27, v27
	v_med3_f32 v199, v199, s87, v227
	v_rcp_f32_e32 v15, v15
	v_med3_f32 v214, v214, s87, v227
	v_exp_f32_e32 v29, v29
	v_pk_fma_f32 v[22:23], v[22:23], v[2:3], v[2:3] op_sel:[0,1,1] op_sel_hi:[1,1,1]
	v_exp_f32_e32 v32, v32
	v_pk_mul_f32 v[8:9], v[104:105], v[2:3] op_sel_hi:[1,0]
	v_rcp_f32_e32 v17, v17
	v_cvt_pk_fp8_f32 v6, v196, v197 op_sel:[0,0,1]
	v_rcp_f32_e32 v19, v19
	v_cvt_pk_fp8_f32 v7, v198, v199
	v_exp_f32_e32 v200, v200
	v_med3_f32 v215, v215, s87, v227
	v_exp_f32_e32 v202, v202
	v_pk_fma_f32 v[24:25], v[24:25], v[2:3], v[2:3] op_sel:[0,1,1] op_sel_hi:[1,1,1]
	v_rcp_f32_e32 v21, v21
	v_pk_fma_f32 v[26:27], v[26:27], v[2:3], v[2:3] op_sel:[0,1,1] op_sel_hi:[1,1,1]
	v_rcp_f32_e32 v22, v22
	v_cvt_pk_fp8_f32 v7, v214, v215 op_sel:[0,0,1]
	v_exp_f32_e32 v8, v8
	v_pk_fma_f32 v[28:29], v[28:29], v[2:3], v[2:3] op_sel:[0,1,1] op_sel_hi:[1,1,1]
	v_rcp_f32_e32 v24, v24
	v_pk_mul_f32 v[10:11], v[142:143], v[138:139]
	v_rcp_f32_e32 v26, v26
	global_store_dwordx2 v249, v[6:7], s[36:37]
	v_pk_mul_f32 v[10:11], v[10:11], v[14:15]
	v_exp_f32_e32 v33, v33
	v_pk_mul_f32 v[6:7], v[94:95], v[2:3] op_sel_hi:[1,0]
	v_med3_f32 v10, v10, s87, v227
	v_rcp_f32_e32 v28, v28
	v_pk_mul_f32 v[12:13], v[144:145], v[140:141]
	v_exp_f32_e32 v201, v201
	v_med3_f32 v11, v11, s87, v227
	v_pk_mul_f32 v[12:13], v[12:13], v[16:17]
	v_exp_f32_e32 v203, v203
	v_pk_mul_f32 v[14:15], v[134:135], v[130:131]
	v_med3_f32 v12, v12, s87, v227
	v_rcp_f32_e32 v23, v23
	v_pk_mul_f32 v[14:15], v[14:15], v[18:19]
	v_exp_f32_e32 v9, v9
	v_pk_mul_f32 v[16:17], v[96:97], v[2:3] op_sel_hi:[1,0]
	v_med3_f32 v14, v14, s87, v227
	v_exp_f32_e32 v6, v6
	v_pk_mul_f32 v[18:19], v[86:87], v[2:3] op_sel_hi:[1,0]
	v_cvt_pk_fp8_f32 v10, v10, v11
	v_med3_f32 v13, v13, s87, v227
	v_med3_f32 v15, v15, s87, v227
	v_pk_mul_f32 v[30:31], v[136:137], v[132:133]
	v_rcp_f32_e32 v25, v25
	v_pk_fma_f32 v[32:33], v[32:33], v[2:3], v[2:3] op_sel:[0,1,1] op_sel_hi:[1,1,1]
	v_pk_mul_f32 v[30:31], v[30:31], v[20:21]
	v_rcp_f32_e32 v27, v27
	v_pk_mul_f32 v[20:21], v[88:89], v[2:3] op_sel_hi:[1,0]
	v_med3_f32 v30, v30, s87, v227
	v_exp_f32_e32 v16, v16
	v_cvt_pk_fp8_f32 v10, v12, v13 op_sel:[0,0,1]
	v_exp_f32_e32 v18, v18
	v_cvt_pk_fp8_f32 v11, v14, v15
	v_med3_f32 v31, v31, s87, v227
	v_rcp_f32_e32 v29, v29
	v_pk_fma_f32 v[200:201], v[200:201], v[2:3], v[2:3] op_sel:[0,1,1] op_sel_hi:[1,1,1]
	v_rcp_f32_e32 v32, v32
	v_pk_fma_f32 v[202:203], v[202:203], v[2:3], v[2:3] op_sel:[0,1,1] op_sel_hi:[1,1,1]
	v_exp_f32_e32 v20, v20
	v_cvt_pk_fp8_f32 v11, v30, v31 op_sel:[0,0,1]
	v_rcp_f32_e32 v200, v200
	v_pk_fma_f32 v[8:9], v[8:9], v[2:3], v[2:3] op_sel:[0,1,1] op_sel_hi:[1,1,1]
	v_rcp_f32_e32 v202, v202
	v_pk_mul_f32 v[12:13], v[126:127], v[122:123]
	v_exp_f32_e32 v7, v7
	v_pk_mul_f32 v[14:15], v[78:79], v[2:3] op_sel_hi:[1,0]
	v_pk_mul_f32 v[12:13], v[12:13], v[22:23]
	v_rcp_f32_e32 v8, v8
	v_pk_mul_f32 v[22:23], v[128:129], v[124:125]
	v_med3_f32 v12, v12, s87, v227
	v_exp_f32_e32 v17, v17
	v_pk_mul_f32 v[22:23], v[22:23], v[24:25]
	v_exp_f32_e32 v19, v19
	v_med3_f32 v13, v13, s87, v227
	v_med3_f32 v22, v22, s87, v227
	v_pk_mul_f32 v[24:25], v[118:119], v[114:115]
	v_rcp_f32_e32 v33, v33
	v_pk_mul_f32 v[30:31], v[80:81], v[2:3] op_sel_hi:[1,0]
	v_pk_mul_f32 v[24:25], v[24:25], v[26:27]
	v_exp_f32_e32 v21, v21
	v_pk_mul_f32 v[26:27], v[70:71], v[2:3] op_sel_hi:[1,0]
	v_med3_f32 v24, v24, s87, v227
	v_exp_f32_e32 v14, v14
	v_cvt_pk_fp8_f32 v12, v12, v13
	v_med3_f32 v23, v23, s87, v227
	v_med3_f32 v25, v25, s87, v227
	v_pk_mul_f32 v[196:197], v[120:121], v[116:117]
	v_rcp_f32_e32 v201, v201
	v_pk_fma_f32 v[6:7], v[6:7], v[2:3], v[2:3] op_sel:[0,1,1] op_sel_hi:[1,1,1]
	v_pk_mul_f32 v[196:197], v[196:197], v[28:29]
	v_rcp_f32_e32 v203, v203
	v_pk_mul_f32 v[28:29], v[72:73], v[2:3] op_sel_hi:[1,0]
	v_med3_f32 v196, v196, s87, v227
	v_exp_f32_e32 v30, v30
	v_cvt_pk_fp8_f32 v12, v22, v23 op_sel:[0,0,1]
	v_exp_f32_e32 v26, v26
	v_cvt_pk_fp8_f32 v13, v24, v25
	v_med3_f32 v197, v197, s87, v227
	v_rcp_f32_e32 v9, v9
	v_pk_fma_f32 v[16:17], v[16:17], v[2:3], v[2:3] op_sel:[0,1,1] op_sel_hi:[1,1,1]
	v_rcp_f32_e32 v6, v6
	v_pk_fma_f32 v[18:19], v[18:19], v[2:3], v[2:3] op_sel:[0,1,1] op_sel_hi:[1,1,1]
	v_exp_f32_e32 v28, v28
	v_cvt_pk_fp8_f32 v13, v196, v197 op_sel:[0,0,1]
	v_rcp_f32_e32 v16, v16
	v_pk_fma_f32 v[20:21], v[20:21], v[2:3], v[2:3] op_sel:[0,1,1] op_sel_hi:[1,1,1]
	v_rcp_f32_e32 v18, v18
	v_pk_mul_f32 v[22:23], v[110:111], v[106:107]
	v_exp_f32_e32 v15, v15
	v_pk_mul_f32 v[24:25], v[62:63], v[2:3] op_sel_hi:[1,0]
	v_pk_mul_f32 v[22:23], v[22:23], v[32:33]
	v_rcp_f32_e32 v20, v20
	v_pk_mul_f32 v[32:33], v[112:113], v[108:109]
	v_med3_f32 v22, v22, s87, v227
	v_exp_f32_e32 v31, v31
	v_pk_mul_f32 v[32:33], v[32:33], v[200:201]
	v_exp_f32_e32 v27, v27
	v_med3_f32 v23, v23, s87, v227
	v_med3_f32 v32, v32, s87, v227
	v_pk_mul_f32 v[196:197], v[102:103], v[98:99]
	v_rcp_f32_e32 v7, v7
	v_add_u32_e32 v198, 0xe000, v249
	v_pk_mul_f32 v[196:197], v[196:197], v[202:203]
	v_exp_f32_e32 v29, v29
	global_store_dwordx2 v198, v[10:11], s[36:37]
	v_med3_f32 v196, v196, s87, v227
	v_exp_f32_e32 v24, v24
	v_pk_mul_f32 v[10:11], v[64:65], v[2:3] op_sel_hi:[1,0]
	v_pk_mul_f32 v[198:199], v[54:55], v[2:3] op_sel_hi:[1,0]
	v_cvt_pk_fp8_f32 v22, v22, v23
	v_med3_f32 v33, v33, s87, v227
	v_med3_f32 v197, v197, s87, v227
	v_pk_mul_f32 v[200:201], v[104:105], v[100:101]
	v_rcp_f32_e32 v17, v17
	v_pk_fma_f32 v[14:15], v[14:15], v[2:3], v[2:3] op_sel:[0,1,1] op_sel_hi:[1,1,1]
	v_pk_mul_f32 v[200:201], v[200:201], v[8:9]
	v_rcp_f32_e32 v19, v19
	v_pk_mul_f32 v[8:9], v[56:57], v[2:3] op_sel_hi:[1,0]
	v_med3_f32 v200, v200, s87, v227
	v_exp_f32_e32 v10, v10
	v_cvt_pk_fp8_f32 v22, v32, v33 op_sel:[0,0,1]
	v_exp_f32_e32 v198, v198
	v_cvt_pk_fp8_f32 v23, v196, v197
	v_med3_f32 v201, v201, s87, v227
	v_rcp_f32_e32 v21, v21
	v_pk_fma_f32 v[30:31], v[30:31], v[2:3], v[2:3] op_sel:[0,1,1] op_sel_hi:[1,1,1]
	v_rcp_f32_e32 v14, v14
	v_pk_fma_f32 v[26:27], v[26:27], v[2:3], v[2:3] op_sel:[0,1,1] op_sel_hi:[1,1,1]
	v_exp_f32_e32 v8, v8
	v_cvt_pk_fp8_f32 v23, v200, v201 op_sel:[0,0,1]
	v_rcp_f32_e32 v30, v30
	v_pk_fma_f32 v[28:29], v[28:29], v[2:3], v[2:3] op_sel:[0,1,1] op_sel_hi:[1,1,1]
	v_rcp_f32_e32 v26, v26
	v_pk_mul_f32 v[32:33], v[94:95], v[90:91]
	v_exp_f32_e32 v25, v25
	v_pk_mul_f32 v[196:197], v[46:47], v[2:3] op_sel_hi:[1,0]
	v_pk_mul_f32 v[32:33], v[32:33], v[6:7]
	v_rcp_f32_e32 v28, v28
	v_pk_mul_f32 v[6:7], v[96:97], v[92:93]
	v_med3_f32 v32, v32, s87, v227
	v_exp_f32_e32 v11, v11
	v_pk_mul_f32 v[6:7], v[6:7], v[16:17]
	v_exp_f32_e32 v199, v199
	v_med3_f32 v33, v33, s87, v227
	v_med3_f32 v6, v6, s87, v227
	v_pk_mul_f32 v[16:17], v[86:87], v[82:83]
	v_rcp_f32_e32 v15, v15
	v_add_u32_e32 v200, 0x1c000, v249
	v_pk_mul_f32 v[16:17], v[16:17], v[18:19]
	v_exp_f32_e32 v9, v9
	global_store_dwordx2 v200, v[12:13], s[36:37]
	v_med3_f32 v16, v16, s87, v227
	v_exp_f32_e32 v196, v196
	v_pk_mul_f32 v[12:13], v[48:49], v[2:3] op_sel_hi:[1,0]
	v_pk_mul_f32 v[18:19], v[38:39], v[2:3] op_sel_hi:[1,0]
	v_cvt_pk_fp8_f32 v32, v32, v33
	v_med3_f32 v7, v7, s87, v227
	v_med3_f32 v17, v17, s87, v227
	v_pk_mul_f32 v[200:201], v[88:89], v[84:85]
	v_rcp_f32_e32 v31, v31
	v_pk_fma_f32 v[24:25], v[24:25], v[2:3], v[2:3] op_sel:[0,1,1] op_sel_hi:[1,1,1]
	v_pk_mul_f32 v[200:201], v[200:201], v[20:21]
	v_rcp_f32_e32 v27, v27
	v_pk_mul_f32 v[20:21], v[40:41], v[2:3] op_sel_hi:[1,0]
	v_med3_f32 v200, v200, s87, v227
	v_exp_f32_e32 v12, v12
	v_cvt_pk_fp8_f32 v32, v6, v7 op_sel:[0,0,1]
	v_exp_f32_e32 v18, v18
	v_cvt_pk_fp8_f32 v33, v16, v17
	v_med3_f32 v201, v201, s87, v227
	v_rcp_f32_e32 v29, v29
	v_pk_fma_f32 v[10:11], v[10:11], v[2:3], v[2:3] op_sel:[0,1,1] op_sel_hi:[1,1,1]
	v_rcp_f32_e32 v24, v24
	v_pk_fma_f32 v[198:199], v[198:199], v[2:3], v[2:3] op_sel:[0,1,1] op_sel_hi:[1,1,1]
	v_exp_f32_e32 v20, v20
	v_cvt_pk_fp8_f32 v33, v200, v201 op_sel:[0,0,1]
	v_rcp_f32_e32 v10, v10
	v_pk_fma_f32 v[8:9], v[8:9], v[2:3], v[2:3] op_sel:[0,1,1] op_sel_hi:[1,1,1]
	v_rcp_f32_e32 v198, v198
	v_pk_mul_f32 v[6:7], v[78:79], v[74:75]
	v_exp_f32_e32 v197, v197
	v_pk_mul_f32 v[16:17], v[80:81], v[76:77]
	v_pk_mul_f32 v[6:7], v[6:7], v[14:15]
	v_rcp_f32_e32 v8, v8
	v_pk_mul_f32 v[16:17], v[16:17], v[30:31]
	v_med3_f32 v6, v6, s87, v227
	v_exp_f32_e32 v13, v13
	v_med3_f32 v16, v16, s87, v227
	v_exp_f32_e32 v19, v19
	v_med3_f32 v7, v7, s87, v227
	v_pk_mul_f32 v[14:15], v[70:71], v[66:67]
	v_rcp_f32_e32 v25, v25
	v_add_u32_e32 v30, 0x2a000, v249
	v_pk_mul_f32 v[14:15], v[14:15], v[26:27]
	v_exp_f32_e32 v21, v21
	global_store_dwordx2 v30, v[22:23], s[36:37]
	v_med3_f32 v14, v14, s87, v227
	v_cvt_pk_fp8_f32 v6, v6, v7
	v_med3_f32 v17, v17, s87, v227
	v_med3_f32 v15, v15, s87, v227
	v_pk_mul_f32 v[22:23], v[72:73], v[68:69]
	v_rcp_f32_e32 v11, v11
	v_pk_fma_f32 v[196:197], v[196:197], v[2:3], v[2:3] op_sel:[0,1,1] op_sel_hi:[1,1,1]
	v_pk_mul_f32 v[22:23], v[22:23], v[28:29]
	v_rcp_f32_e32 v199, v199
	v_cvt_pk_fp8_f32 v6, v16, v17 op_sel:[0,0,1]
	v_med3_f32 v22, v22, s87, v227
	v_cvt_pk_fp8_f32 v7, v14, v15
	v_rcp_f32_e32 v9, v9
	v_med3_f32 v23, v23, s87, v227
	v_rcp_f32_e32 v196, v196
	v_pk_fma_f32 v[12:13], v[12:13], v[2:3], v[2:3] op_sel:[0,1,1] op_sel_hi:[1,1,1]
	v_pk_fma_f32 v[18:19], v[18:19], v[2:3], v[2:3] op_sel:[0,1,1] op_sel_hi:[1,1,1]
	v_cvt_pk_fp8_f32 v7, v22, v23 op_sel:[0,0,1]
	v_rcp_f32_e32 v12, v12
	v_pk_fma_f32 v[20:21], v[20:21], v[2:3], v[2:3] op_sel:[0,1,1] op_sel_hi:[1,1,1]
	v_rcp_f32_e32 v18, v18
	v_pk_mul_f32 v[14:15], v[62:63], v[58:59]
	v_rcp_f32_e32 v20, v20
	v_pk_mul_f32 v[16:17], v[64:65], v[60:61]
	v_pk_mul_f32 v[14:15], v[14:15], v[24:25]
	v_pk_mul_f32 v[22:23], v[54:55], v[50:51]
	v_pk_mul_f32 v[16:17], v[16:17], v[10:11]
	v_med3_f32 v14, v14, s87, v227
	v_pk_mul_f32 v[22:23], v[22:23], v[198:199]
	v_med3_f32 v16, v16, s87, v227
	v_med3_f32 v15, v15, s87, v227
	v_med3_f32 v22, v22, s87, v227
	v_rcp_f32_e32 v197, v197
	v_add_u32_e32 v10, 0x70000, v249
	v_cvt_pk_fp8_f32 v14, v14, v15
	v_med3_f32 v17, v17, s87, v227
	global_store_dwordx2 v10, v[32:33], s[36:37]
	v_med3_f32 v23, v23, s87, v227
	v_pk_mul_f32 v[10:11], v[56:57], v[52:53]
	v_rcp_f32_e32 v13, v13
	v_cvt_pk_fp8_f32 v14, v16, v17 op_sel:[0,0,1]
	v_pk_mul_f32 v[10:11], v[10:11], v[8:9]
	v_rcp_f32_e32 v19, v19
	v_cvt_pk_fp8_f32 v15, v22, v23
	v_med3_f32 v10, v10, s87, v227
	v_rcp_f32_e32 v21, v21
	v_pk_mul_f32 v[8:9], v[46:47], v[42:43]
	v_med3_f32 v11, v11, s87, v227
	v_pk_mul_f32 v[16:17], v[48:49], v[44:45]
	v_pk_mul_f32 v[8:9], v[8:9], v[196:197]
	v_cvt_pk_fp8_f32 v15, v10, v11 op_sel:[0,0,1]
	v_pk_mul_f32 v[16:17], v[16:17], v[12:13]
	v_med3_f32 v8, v8, s87, v227
	v_pk_mul_f32 v[10:11], v[38:39], v[34:35]
	v_med3_f32 v16, v16, s87, v227
	v_med3_f32 v9, v9, s87, v227
	v_pk_mul_f32 v[10:11], v[10:11], v[18:19]
	v_add_u32_e32 v12, 0x7e000, v249
	v_cvt_pk_fp8_f32 v8, v8, v9
	v_med3_f32 v10, v10, s87, v227
	global_store_dwordx2 v12, v[6:7], s[36:37]
	v_med3_f32 v17, v17, s87, v227
	v_med3_f32 v11, v11, s87, v227
	v_pk_mul_f32 v[6:7], v[40:41], v[36:37]
	v_cvt_pk_fp8_f32 v8, v16, v17 op_sel:[0,0,1]
	v_cvt_pk_fp8_f32 v9, v10, v11
	v_pk_mul_f32 v[6:7], v[6:7], v[20:21]
	v_add_u32_e32 v10, 0x8c000, v249
	v_add_u32_e32 v11, 0x9a000, v249
	v_med3_f32 v6, v6, s87, v227
	global_store_dwordx2 v10, v[14:15], s[36:37]
	v_med3_f32 v7, v7, s87, v227
	v_cvt_pk_fp8_f32 v9, v6, v7 op_sel:[0,0,1]
	global_store_dwordx2 v11, v[8:9], s[36:37]
	s_and_b64 vcc, exec, s[38:39]
	s_mov_b64 s[38:39], -1
	s_cbranch_vccnz .LBB0_1675
	s_andn2_b64 vcc, exec, s[34:35]
	s_cbranch_vccnz .LBB0_1674
	s_barrier
	s_branch .LBB0_1674

.LBB0_1843:
	v_mov_b32_e32 v2, 0xbfb8aa3b
	v_mov_b32_e32 v3, 0x3e000000
	v_mov_b32_e32 v4, 0x41000000
	v_lshl_add_u32 v251, s58, 8, v209
	v_lshl_or_b32 v250, s54, 7, v211
	v_mad_u32_u24 v249, v251, s33, v250
	v_pk_mul_f32 v[6:7], v[154:155], v[2:3] op_sel_hi:[1,0]
	v_pk_mul_f32 v[8:9], v[156:157], v[2:3] op_sel_hi:[1,0]
	v_pk_mul_f32 v[10:11], v[150:151], v[2:3] op_sel_hi:[1,0]
	v_exp_f32_e32 v6, v6
	v_pk_mul_f32 v[12:13], v[152:153], v[2:3] op_sel_hi:[1,0]
	v_exp_f32_e32 v8, v8
	v_pk_mul_f32 v[14:15], v[142:143], v[2:3] op_sel_hi:[1,0]
	v_exp_f32_e32 v10, v10
	v_pk_mul_f32 v[16:17], v[144:145], v[2:3] op_sel_hi:[1,0]
	v_exp_f32_e32 v12, v12
	v_pk_mul_f32 v[18:19], v[134:135], v[2:3] op_sel_hi:[1,0]
	v_exp_f32_e32 v7, v7
	v_pk_mul_f32 v[20:21], v[136:137], v[2:3] op_sel_hi:[1,0]
	v_exp_f32_e32 v9, v9
	v_pk_mul_f32 v[22:23], v[126:127], v[2:3] op_sel_hi:[1,0]
	v_exp_f32_e32 v11, v11
	v_pk_mul_f32 v[24:25], v[128:129], v[2:3] op_sel_hi:[1,0]
	v_exp_f32_e32 v13, v13
	v_pk_mul_f32 v[26:27], v[118:119], v[2:3] op_sel_hi:[1,0]
	v_exp_f32_e32 v14, v14
	v_pk_fma_f32 v[6:7], v[6:7], v[2:3], v[2:3] op_sel:[0,1,1] op_sel_hi:[1,1,1]
	v_exp_f32_e32 v16, v16
	v_pk_fma_f32 v[8:9], v[8:9], v[2:3], v[2:3] op_sel:[0,1,1] op_sel_hi:[1,1,1]
	v_exp_f32_e32 v18, v18
	v_pk_fma_f32 v[10:11], v[10:11], v[2:3], v[2:3] op_sel:[0,1,1] op_sel_hi:[1,1,1]
	v_rcp_f32_e32 v6, v6
	v_pk_fma_f32 v[12:13], v[12:13], v[2:3], v[2:3] op_sel:[0,1,1] op_sel_hi:[1,1,1]
	v_exp_f32_e32 v20, v20
	v_pk_mul_f32 v[28:29], v[120:121], v[2:3] op_sel_hi:[1,0]
	v_rcp_f32_e32 v8, v8
	v_pk_mul_f32 v[30:31], v[154:155], v[158:159]
	v_rcp_f32_e32 v10, v10
	v_pk_mul_f32 v[32:33], v[110:111], v[2:3] op_sel_hi:[1,0]
	v_exp_f32_e32 v15, v15
	v_pk_mul_f32 v[196:197], v[156:157], v[160:161]
	v_rcp_f32_e32 v12, v12
	v_pk_mul_f32 v[198:199], v[150:151], v[146:147]
	v_exp_f32_e32 v17, v17
	v_pk_mul_f32 v[200:201], v[112:113], v[2:3] op_sel_hi:[1,0]
	v_exp_f32_e32 v19, v19
	v_pk_mul_f32 v[202:203], v[102:103], v[2:3] op_sel_hi:[1,0]
	v_rcp_f32_e32 v7, v7
	v_pk_fma_f32 v[14:15], v[14:15], v[2:3], v[2:3] op_sel:[0,1,1] op_sel_hi:[1,1,1]
	v_exp_f32_e32 v21, v21
	v_pk_mul_f32 v[214:215], v[152:153], v[148:149]
	v_exp_f32_e32 v22, v22
	v_pk_fma_f32 v[16:17], v[16:17], v[2:3], v[2:3] op_sel:[0,1,1] op_sel_hi:[1,1,1]
	v_rcp_f32_e32 v9, v9
	v_pk_fma_f32 v[18:19], v[18:19], v[2:3], v[2:3] op_sel:[0,1,1] op_sel_hi:[1,1,1]
	v_rcp_f32_e32 v11, v11
	v_pk_mul_f32 v[30:31], v[30:31], v[6:7]
	v_exp_f32_e32 v24, v24
	v_pk_fma_f32 v[20:21], v[20:21], v[2:3], v[2:3] op_sel:[0,1,1] op_sel_hi:[1,1,1]
	v_exp_f32_e32 v26, v26
	v_med3_f32 v30, v30, s87, v227
	v_rcp_f32_e32 v13, v13
	v_pk_mul_f32 v[196:197], v[196:197], v[8:9]
	v_rcp_f32_e32 v14, v14
	v_pk_mul_f32 v[198:199], v[198:199], v[10:11]
	v_exp_f32_e32 v28, v28
	v_med3_f32 v31, v31, s87, v227
	v_rcp_f32_e32 v16, v16
	v_med3_f32 v196, v196, s87, v227
	v_rcp_f32_e32 v18, v18
	v_med3_f32 v198, v198, s87, v227
	v_exp_f32_e32 v23, v23
	v_pk_mul_f32 v[214:215], v[214:215], v[12:13]
	v_rcp_f32_e32 v20, v20
	v_cvt_pk_fp8_f32 v6, v30, v31
	v_exp_f32_e32 v25, v25
	v_med3_f32 v197, v197, s87, v227
	v_exp_f32_e32 v27, v27
	v_med3_f32 v199, v199, s87, v227
	v_rcp_f32_e32 v15, v15
	v_med3_f32 v214, v214, s87, v227
	v_exp_f32_e32 v29, v29
	v_pk_fma_f32 v[22:23], v[22:23], v[2:3], v[2:3] op_sel:[0,1,1] op_sel_hi:[1,1,1]
	v_exp_f32_e32 v32, v32
	v_pk_mul_f32 v[8:9], v[104:105], v[2:3] op_sel_hi:[1,0]
	v_rcp_f32_e32 v17, v17
	v_cvt_pk_fp8_f32 v6, v196, v197 op_sel:[0,0,1]
	v_rcp_f32_e32 v19, v19
	v_cvt_pk_fp8_f32 v7, v198, v199
	v_exp_f32_e32 v200, v200
	v_med3_f32 v215, v215, s87, v227
	v_exp_f32_e32 v202, v202
	v_pk_fma_f32 v[24:25], v[24:25], v[2:3], v[2:3] op_sel:[0,1,1] op_sel_hi:[1,1,1]
	v_rcp_f32_e32 v21, v21
	v_pk_fma_f32 v[26:27], v[26:27], v[2:3], v[2:3] op_sel:[0,1,1] op_sel_hi:[1,1,1]
	v_rcp_f32_e32 v22, v22
	v_cvt_pk_fp8_f32 v7, v214, v215 op_sel:[0,0,1]
	v_exp_f32_e32 v8, v8
	v_pk_fma_f32 v[28:29], v[28:29], v[2:3], v[2:3] op_sel:[0,1,1] op_sel_hi:[1,1,1]
	v_rcp_f32_e32 v24, v24
	v_pk_mul_f32 v[10:11], v[142:143], v[138:139]
	v_rcp_f32_e32 v26, v26
	global_store_dwordx2 v249, v[6:7], s[36:37]
	v_pk_mul_f32 v[10:11], v[10:11], v[14:15]
	v_exp_f32_e32 v33, v33
	v_pk_mul_f32 v[6:7], v[94:95], v[2:3] op_sel_hi:[1,0]
	v_med3_f32 v10, v10, s87, v227
	v_rcp_f32_e32 v28, v28
	v_pk_mul_f32 v[12:13], v[144:145], v[140:141]
	v_exp_f32_e32 v201, v201
	v_med3_f32 v11, v11, s87, v227
	v_pk_mul_f32 v[12:13], v[12:13], v[16:17]
	v_exp_f32_e32 v203, v203
	v_pk_mul_f32 v[14:15], v[134:135], v[130:131]
	v_med3_f32 v12, v12, s87, v227
	v_rcp_f32_e32 v23, v23
	v_pk_mul_f32 v[14:15], v[14:15], v[18:19]
	v_exp_f32_e32 v9, v9
	v_pk_mul_f32 v[16:17], v[96:97], v[2:3] op_sel_hi:[1,0]
	v_med3_f32 v14, v14, s87, v227
	v_exp_f32_e32 v6, v6
	v_pk_mul_f32 v[18:19], v[86:87], v[2:3] op_sel_hi:[1,0]
	v_cvt_pk_fp8_f32 v10, v10, v11
	v_med3_f32 v13, v13, s87, v227
	v_med3_f32 v15, v15, s87, v227
	v_pk_mul_f32 v[30:31], v[136:137], v[132:133]
	v_rcp_f32_e32 v25, v25
	v_pk_fma_f32 v[32:33], v[32:33], v[2:3], v[2:3] op_sel:[0,1,1] op_sel_hi:[1,1,1]
	v_pk_mul_f32 v[30:31], v[30:31], v[20:21]
	v_rcp_f32_e32 v27, v27
	v_pk_mul_f32 v[20:21], v[88:89], v[2:3] op_sel_hi:[1,0]
	v_med3_f32 v30, v30, s87, v227
	v_exp_f32_e32 v16, v16
	v_cvt_pk_fp8_f32 v10, v12, v13 op_sel:[0,0,1]
	v_exp_f32_e32 v18, v18
	v_cvt_pk_fp8_f32 v11, v14, v15
	v_med3_f32 v31, v31, s87, v227
	v_rcp_f32_e32 v29, v29
	v_pk_fma_f32 v[200:201], v[200:201], v[2:3], v[2:3] op_sel:[0,1,1] op_sel_hi:[1,1,1]
	v_rcp_f32_e32 v32, v32
	v_pk_fma_f32 v[202:203], v[202:203], v[2:3], v[2:3] op_sel:[0,1,1] op_sel_hi:[1,1,1]
	v_exp_f32_e32 v20, v20
	v_cvt_pk_fp8_f32 v11, v30, v31 op_sel:[0,0,1]
	v_rcp_f32_e32 v200, v200
	v_pk_fma_f32 v[8:9], v[8:9], v[2:3], v[2:3] op_sel:[0,1,1] op_sel_hi:[1,1,1]
	v_rcp_f32_e32 v202, v202
	v_pk_mul_f32 v[12:13], v[126:127], v[122:123]
	v_exp_f32_e32 v7, v7
	v_pk_mul_f32 v[14:15], v[78:79], v[2:3] op_sel_hi:[1,0]
	v_pk_mul_f32 v[12:13], v[12:13], v[22:23]
	v_rcp_f32_e32 v8, v8
	v_pk_mul_f32 v[22:23], v[128:129], v[124:125]
	v_med3_f32 v12, v12, s87, v227
	v_exp_f32_e32 v17, v17
	v_pk_mul_f32 v[22:23], v[22:23], v[24:25]
	v_exp_f32_e32 v19, v19
	v_med3_f32 v13, v13, s87, v227
	v_med3_f32 v22, v22, s87, v227
	v_pk_mul_f32 v[24:25], v[118:119], v[114:115]
	v_rcp_f32_e32 v33, v33
	v_pk_mul_f32 v[30:31], v[80:81], v[2:3] op_sel_hi:[1,0]
	v_pk_mul_f32 v[24:25], v[24:25], v[26:27]
	v_exp_f32_e32 v21, v21
	v_pk_mul_f32 v[26:27], v[70:71], v[2:3] op_sel_hi:[1,0]
	v_med3_f32 v24, v24, s87, v227
	v_exp_f32_e32 v14, v14
	v_cvt_pk_fp8_f32 v12, v12, v13
	v_med3_f32 v23, v23, s87, v227
	v_med3_f32 v25, v25, s87, v227
	v_pk_mul_f32 v[196:197], v[120:121], v[116:117]
	v_rcp_f32_e32 v201, v201
	v_pk_fma_f32 v[6:7], v[6:7], v[2:3], v[2:3] op_sel:[0,1,1] op_sel_hi:[1,1,1]
	v_pk_mul_f32 v[196:197], v[196:197], v[28:29]
	v_rcp_f32_e32 v203, v203
	v_pk_mul_f32 v[28:29], v[72:73], v[2:3] op_sel_hi:[1,0]
	v_med3_f32 v196, v196, s87, v227
	v_exp_f32_e32 v30, v30
	v_cvt_pk_fp8_f32 v12, v22, v23 op_sel:[0,0,1]
	v_exp_f32_e32 v26, v26
	v_cvt_pk_fp8_f32 v13, v24, v25
	v_med3_f32 v197, v197, s87, v227
	v_rcp_f32_e32 v9, v9
	v_pk_fma_f32 v[16:17], v[16:17], v[2:3], v[2:3] op_sel:[0,1,1] op_sel_hi:[1,1,1]
	v_rcp_f32_e32 v6, v6
	v_pk_fma_f32 v[18:19], v[18:19], v[2:3], v[2:3] op_sel:[0,1,1] op_sel_hi:[1,1,1]
	v_exp_f32_e32 v28, v28
	v_cvt_pk_fp8_f32 v13, v196, v197 op_sel:[0,0,1]
	v_rcp_f32_e32 v16, v16
	v_pk_fma_f32 v[20:21], v[20:21], v[2:3], v[2:3] op_sel:[0,1,1] op_sel_hi:[1,1,1]
	v_rcp_f32_e32 v18, v18
	v_pk_mul_f32 v[22:23], v[110:111], v[106:107]
	v_exp_f32_e32 v15, v15
	v_pk_mul_f32 v[24:25], v[62:63], v[2:3] op_sel_hi:[1,0]
	v_pk_mul_f32 v[22:23], v[22:23], v[32:33]
	v_rcp_f32_e32 v20, v20
	v_pk_mul_f32 v[32:33], v[112:113], v[108:109]
	v_med3_f32 v22, v22, s87, v227
	v_exp_f32_e32 v31, v31
	v_pk_mul_f32 v[32:33], v[32:33], v[200:201]
	v_exp_f32_e32 v27, v27
	v_med3_f32 v23, v23, s87, v227
	v_med3_f32 v32, v32, s87, v227
	v_pk_mul_f32 v[196:197], v[102:103], v[98:99]
	v_rcp_f32_e32 v7, v7
	v_add_u32_e32 v198, 0xe000, v249
	v_pk_mul_f32 v[196:197], v[196:197], v[202:203]
	v_exp_f32_e32 v29, v29
	global_store_dwordx2 v198, v[10:11], s[36:37]
	v_med3_f32 v196, v196, s87, v227
	v_exp_f32_e32 v24, v24
	v_pk_mul_f32 v[10:11], v[64:65], v[2:3] op_sel_hi:[1,0]
	v_pk_mul_f32 v[198:199], v[54:55], v[2:3] op_sel_hi:[1,0]
	v_cvt_pk_fp8_f32 v22, v22, v23
	v_med3_f32 v33, v33, s87, v227
	v_med3_f32 v197, v197, s87, v227
	v_pk_mul_f32 v[200:201], v[104:105], v[100:101]
	v_rcp_f32_e32 v17, v17
	v_pk_fma_f32 v[14:15], v[14:15], v[2:3], v[2:3] op_sel:[0,1,1] op_sel_hi:[1,1,1]
	v_pk_mul_f32 v[200:201], v[200:201], v[8:9]
	v_rcp_f32_e32 v19, v19
	v_pk_mul_f32 v[8:9], v[56:57], v[2:3] op_sel_hi:[1,0]
	v_med3_f32 v200, v200, s87, v227
	v_exp_f32_e32 v10, v10
	v_cvt_pk_fp8_f32 v22, v32, v33 op_sel:[0,0,1]
	v_exp_f32_e32 v198, v198
	v_cvt_pk_fp8_f32 v23, v196, v197
	v_med3_f32 v201, v201, s87, v227
	v_rcp_f32_e32 v21, v21
	v_pk_fma_f32 v[30:31], v[30:31], v[2:3], v[2:3] op_sel:[0,1,1] op_sel_hi:[1,1,1]
	v_rcp_f32_e32 v14, v14
	v_pk_fma_f32 v[26:27], v[26:27], v[2:3], v[2:3] op_sel:[0,1,1] op_sel_hi:[1,1,1]
	v_exp_f32_e32 v8, v8
	v_cvt_pk_fp8_f32 v23, v200, v201 op_sel:[0,0,1]
	v_rcp_f32_e32 v30, v30
	v_pk_fma_f32 v[28:29], v[28:29], v[2:3], v[2:3] op_sel:[0,1,1] op_sel_hi:[1,1,1]
	v_rcp_f32_e32 v26, v26
	v_pk_mul_f32 v[32:33], v[94:95], v[90:91]
	v_exp_f32_e32 v25, v25
	v_pk_mul_f32 v[196:197], v[46:47], v[2:3] op_sel_hi:[1,0]
	v_pk_mul_f32 v[32:33], v[32:33], v[6:7]
	v_rcp_f32_e32 v28, v28
	v_pk_mul_f32 v[6:7], v[96:97], v[92:93]
	v_med3_f32 v32, v32, s87, v227
	v_exp_f32_e32 v11, v11
	v_pk_mul_f32 v[6:7], v[6:7], v[16:17]
	v_exp_f32_e32 v199, v199
	v_med3_f32 v33, v33, s87, v227
	v_med3_f32 v6, v6, s87, v227
	v_pk_mul_f32 v[16:17], v[86:87], v[82:83]
	v_rcp_f32_e32 v15, v15
	v_add_u32_e32 v200, 0x1c000, v249
	v_pk_mul_f32 v[16:17], v[16:17], v[18:19]
	v_exp_f32_e32 v9, v9
	global_store_dwordx2 v200, v[12:13], s[36:37]
	v_med3_f32 v16, v16, s87, v227
	v_exp_f32_e32 v196, v196
	v_pk_mul_f32 v[12:13], v[48:49], v[2:3] op_sel_hi:[1,0]
	v_pk_mul_f32 v[18:19], v[38:39], v[2:3] op_sel_hi:[1,0]
	v_cvt_pk_fp8_f32 v32, v32, v33
	v_med3_f32 v7, v7, s87, v227
	v_med3_f32 v17, v17, s87, v227
	v_pk_mul_f32 v[200:201], v[88:89], v[84:85]
	v_rcp_f32_e32 v31, v31
	v_pk_fma_f32 v[24:25], v[24:25], v[2:3], v[2:3] op_sel:[0,1,1] op_sel_hi:[1,1,1]
	v_pk_mul_f32 v[200:201], v[200:201], v[20:21]
	v_rcp_f32_e32 v27, v27
	v_pk_mul_f32 v[20:21], v[40:41], v[2:3] op_sel_hi:[1,0]
	v_med3_f32 v200, v200, s87, v227
	v_exp_f32_e32 v12, v12
	v_cvt_pk_fp8_f32 v32, v6, v7 op_sel:[0,0,1]
	v_exp_f32_e32 v18, v18
	v_cvt_pk_fp8_f32 v33, v16, v17
	v_med3_f32 v201, v201, s87, v227
	v_rcp_f32_e32 v29, v29
	v_pk_fma_f32 v[10:11], v[10:11], v[2:3], v[2:3] op_sel:[0,1,1] op_sel_hi:[1,1,1]
	v_rcp_f32_e32 v24, v24
	v_pk_fma_f32 v[198:199], v[198:199], v[2:3], v[2:3] op_sel:[0,1,1] op_sel_hi:[1,1,1]
	v_exp_f32_e32 v20, v20
	v_cvt_pk_fp8_f32 v33, v200, v201 op_sel:[0,0,1]
	v_rcp_f32_e32 v10, v10
	v_pk_fma_f32 v[8:9], v[8:9], v[2:3], v[2:3] op_sel:[0,1,1] op_sel_hi:[1,1,1]
	v_rcp_f32_e32 v198, v198
	v_pk_mul_f32 v[6:7], v[78:79], v[74:75]
	v_exp_f32_e32 v197, v197
	v_pk_mul_f32 v[16:17], v[80:81], v[76:77]
	v_pk_mul_f32 v[6:7], v[6:7], v[14:15]
	v_rcp_f32_e32 v8, v8
	v_pk_mul_f32 v[16:17], v[16:17], v[30:31]
	v_med3_f32 v6, v6, s87, v227
	v_exp_f32_e32 v13, v13
	v_med3_f32 v16, v16, s87, v227
	v_exp_f32_e32 v19, v19
	v_med3_f32 v7, v7, s87, v227
	v_pk_mul_f32 v[14:15], v[70:71], v[66:67]
	v_rcp_f32_e32 v25, v25
	v_add_u32_e32 v30, 0x2a000, v249
	v_pk_mul_f32 v[14:15], v[14:15], v[26:27]
	v_exp_f32_e32 v21, v21
	global_store_dwordx2 v30, v[22:23], s[36:37]
	v_med3_f32 v14, v14, s87, v227
	v_cvt_pk_fp8_f32 v6, v6, v7
	v_med3_f32 v17, v17, s87, v227
	v_med3_f32 v15, v15, s87, v227
	v_pk_mul_f32 v[22:23], v[72:73], v[68:69]
	v_rcp_f32_e32 v11, v11
	v_pk_fma_f32 v[196:197], v[196:197], v[2:3], v[2:3] op_sel:[0,1,1] op_sel_hi:[1,1,1]
	v_pk_mul_f32 v[22:23], v[22:23], v[28:29]
	v_rcp_f32_e32 v199, v199
	v_cvt_pk_fp8_f32 v6, v16, v17 op_sel:[0,0,1]
	v_med3_f32 v22, v22, s87, v227
	v_cvt_pk_fp8_f32 v7, v14, v15
	v_rcp_f32_e32 v9, v9
	v_med3_f32 v23, v23, s87, v227
	v_rcp_f32_e32 v196, v196
	v_pk_fma_f32 v[12:13], v[12:13], v[2:3], v[2:3] op_sel:[0,1,1] op_sel_hi:[1,1,1]
	v_pk_fma_f32 v[18:19], v[18:19], v[2:3], v[2:3] op_sel:[0,1,1] op_sel_hi:[1,1,1]
	v_cvt_pk_fp8_f32 v7, v22, v23 op_sel:[0,0,1]
	v_rcp_f32_e32 v12, v12
	v_pk_fma_f32 v[20:21], v[20:21], v[2:3], v[2:3] op_sel:[0,1,1] op_sel_hi:[1,1,1]
	v_rcp_f32_e32 v18, v18
	v_pk_mul_f32 v[14:15], v[62:63], v[58:59]
	v_rcp_f32_e32 v20, v20
	v_pk_mul_f32 v[16:17], v[64:65], v[60:61]
	v_pk_mul_f32 v[14:15], v[14:15], v[24:25]
	v_pk_mul_f32 v[22:23], v[54:55], v[50:51]
	v_pk_mul_f32 v[16:17], v[16:17], v[10:11]
	v_med3_f32 v14, v14, s87, v227
	v_pk_mul_f32 v[22:23], v[22:23], v[198:199]
	v_med3_f32 v16, v16, s87, v227
	v_med3_f32 v15, v15, s87, v227
	v_med3_f32 v22, v22, s87, v227
	v_rcp_f32_e32 v197, v197
	v_add_u32_e32 v10, 0x70000, v249
	v_cvt_pk_fp8_f32 v14, v14, v15
	v_med3_f32 v17, v17, s87, v227
	global_store_dwordx2 v10, v[32:33], s[36:37]
	v_med3_f32 v23, v23, s87, v227
	v_pk_mul_f32 v[10:11], v[56:57], v[52:53]
	v_rcp_f32_e32 v13, v13
	v_cvt_pk_fp8_f32 v14, v16, v17 op_sel:[0,0,1]
	v_pk_mul_f32 v[10:11], v[10:11], v[8:9]
	v_rcp_f32_e32 v19, v19
	v_cvt_pk_fp8_f32 v15, v22, v23
	v_med3_f32 v10, v10, s87, v227
	v_rcp_f32_e32 v21, v21
	v_pk_mul_f32 v[8:9], v[46:47], v[42:43]
	v_med3_f32 v11, v11, s87, v227
	v_pk_mul_f32 v[16:17], v[48:49], v[44:45]
	v_pk_mul_f32 v[8:9], v[8:9], v[196:197]
	v_cvt_pk_fp8_f32 v15, v10, v11 op_sel:[0,0,1]
	v_pk_mul_f32 v[16:17], v[16:17], v[12:13]
	v_med3_f32 v8, v8, s87, v227
	v_pk_mul_f32 v[10:11], v[38:39], v[34:35]
	v_med3_f32 v16, v16, s87, v227
	v_med3_f32 v9, v9, s87, v227
	v_pk_mul_f32 v[10:11], v[10:11], v[18:19]
	v_add_u32_e32 v12, 0x7e000, v249
	v_cvt_pk_fp8_f32 v8, v8, v9
	v_med3_f32 v10, v10, s87, v227
	global_store_dwordx2 v12, v[6:7], s[36:37]
	v_med3_f32 v17, v17, s87, v227
	v_med3_f32 v11, v11, s87, v227
	v_pk_mul_f32 v[6:7], v[40:41], v[36:37]
	v_cvt_pk_fp8_f32 v8, v16, v17 op_sel:[0,0,1]
	v_cvt_pk_fp8_f32 v9, v10, v11
	v_pk_mul_f32 v[6:7], v[6:7], v[20:21]
	v_add_u32_e32 v10, 0x8c000, v249
	v_add_u32_e32 v11, 0x9a000, v249
	v_med3_f32 v6, v6, s87, v227
	global_store_dwordx2 v10, v[14:15], s[36:37]
	v_med3_f32 v7, v7, s87, v227
	v_cvt_pk_fp8_f32 v9, v6, v7 op_sel:[0,0,1]
	global_store_dwordx2 v11, v[8:9], s[36:37]
	s_mov_b64 s[54:55], -1
	s_and_b64 vcc, exec, s[50:51]
	s_cbranch_vccz .LBB0_1818
	s_andn2_b64 vcc, exec, s[34:35]
	s_cbranch_vccnz .LBB0_1817
	s_barrier
	s_branch .LBB0_1817
